# speedup vs baseline: 1.0008x; 1.0008x over previous
_Z10ode_kernelPKfPKDF16_S2_PfPKi:
	v_lshrrev_b32_e32 v167, 6, v0
	s_lshr_b32 s3, s2, 3
	v_add_u32_e32 v2, s3, v167
	s_load_dwordx4 s[4:7], s[0:1], 0x0
	s_load_dwordx2 s[12:13], s[0:1], 0x10
	v_and_b32_e32 v130, 3, v2
	v_and_b32_e32 v1, 63, v0
	v_readfirstlane_b32 s3, v130
	v_lshlrev_b32_e32 v166, 4, v1
	s_lshl_b32 s11, s3, 14
	v_lshl_or_b32 v2, v130, 17, v166
	v_mov_b32_e32 v3, 0
	s_and_b32 s17, s11, 0xc000
	s_mov_b32 s9, 0
	s_waitcnt lgkmcnt(0)
	v_lshl_add_u64 v[74:75], s[6:7], 0, v[2:3]
	s_lshl_b32 s8, s17, 1
	v_lshl_add_u64 v[46:47], v[74:75], 0, s[8:9]
	s_movk_i32 s15, 0x1000
	v_add_co_u32_e32 v18, vcc, s15, v46
	s_movk_i32 s14, 0x3000
	s_nop 0
	v_addc_co_u32_e32 v19, vcc, 0, v47, vcc
	v_add_co_u32_e32 v20, vcc, s14, v46
	s_lshl_b32 s10, s2, 10
	s_nop 0
	v_addc_co_u32_e32 v21, vcc, 0, v47, vcc
	s_and_b32 s8, s10, 0x3e000
	s_movk_i32 s16, 0x7000
	v_add_co_u32_e32 v48, vcc, s16, v46
	v_lshl_or_b32 v22, v1, 7, s8
	s_add_i32 s8, s11, 0x4000
	v_addc_co_u32_e32 v49, vcc, 0, v47, vcc
	s_movk_i32 s16, 0x5000
	s_and_b32 s8, s8, 0xc000
	v_add_co_u32_e32 v50, vcc, s16, v46
	s_lshl_b32 s8, s8, 1
	global_load_dwordx4 v[34:37], v[18:19], off offset:2048
	global_load_dwordx4 v[14:17], v[20:21], off offset:2048
	global_load_dwordx4 v[6:9], v[20:21], off offset:1024
	global_load_dwordx4 v[2:5], v[18:19], off offset:1024
	global_load_dwordx4 v[42:45], v[18:19], off offset:3072
	global_load_dwordx4 v[38:41], v[20:21], off offset:3072
	v_addc_co_u32_e32 v51, vcc, 0, v47, vcc
	v_lshl_add_u64 v[72:73], v[74:75], 0, s[8:9]
	v_add_co_u32_e32 v106, vcc, s14, v72
	global_load_dwordx4 v[10:13], v[50:51], off offset:1024
	global_load_dwordx4 v[52:55], v[50:51], off offset:2048
	global_load_dwordx4 v[56:59], v[48:49], off offset:2048
	v_addc_co_u32_e32 v107, vcc, 0, v73, vcc
	v_add_co_u32_e32 v108, vcc, s15, v72
	global_load_dwordx4 v[60:63], v[50:51], off offset:3072
	global_load_dwordx4 v[64:67], v[48:49], off offset:3072
	global_load_ushort v198, v22, s[12:13]
	v_addc_co_u32_e32 v109, vcc, 0, v73, vcc
	global_load_dwordx4 v[68:71], v[108:109], off offset:2048
	global_load_dwordx4 v[78:81], v[106:107], off offset:2048
	global_load_dwordx4 v[82:85], v[106:107], off offset:3072
	global_load_dwordx4 v[86:89], v[108:109], off offset:3072
	s_add_i32 s8, s11, 0x6000
	s_movk_i32 s16, 0x2000
	s_and_b32 s8, s8, 0xe000
	v_add_co_u32_e32 v26, vcc, s16, v46
	s_lshl_b32 s8, s8, 1
	s_nop 0
	v_addc_co_u32_e32 v27, vcc, 0, v47, vcc
	v_lshl_add_u64 v[110:111], v[74:75], 0, s[8:9]
	v_add_co_u32_e32 v112, vcc, s14, v110
	global_load_dwordx4 a[0:3], v[46:47], off
	global_load_dwordx4 a[8:11], v[46:47], off offset:1024
	global_load_dwordx4 a[12:15], v[26:27], off offset:1024
	global_load_dwordx4 a[20:23], v[26:27], off offset:2048
	global_load_dwordx4 a[16:19], v[46:47], off offset:2048
	global_load_dwordx4 a[24:27], v[46:47], off offset:3072
	global_load_dwordx4 a[4:7], v[20:21], off offset:-4096
	global_load_dwordx4 v[22:25], v[20:21], off
	global_load_dwordx4 a[28:31], v[26:27], off offset:3072
	s_nop 0
	global_load_dwordx4 v[18:21], v[18:19], off
	v_addc_co_u32_e32 v113, vcc, 0, v111, vcc
	v_add_co_u32_e32 v114, vcc, s15, v110
	v_lshl_or_b32 v199, v167, 15, v166
	s_nop 0
	v_addc_co_u32_e32 v115, vcc, 0, v111, vcc
	global_load_dwordx4 v[26:29], v[114:115], off offset:1024
	global_load_dwordx4 v[90:93], v[114:115], off offset:2048
	global_load_dwordx4 v[30:33], v[112:113], off offset:1024
	global_load_dwordx4 v[94:97], v[112:113], off offset:2048
	global_load_dwordx4 v[98:101], v[114:115], off offset:3072
	global_load_dwordx4 v[102:105], v[112:113], off offset:3072
	s_movk_i32 s8, 0x6000
	s_load_dwordx2 s[6:7], s[0:1], 0x20
	v_lshlrev_b32_e32 v76, 1, v0
	v_and_b32_e32 v200, 7, v0
	v_and_b32_e32 v128, 64, v76
	v_and_b32_e32 v179, 15, v0
	v_bfe_u32 v201, v0, 4, 1
	v_mov_b32_e32 v196, 0x44444444
	global_load_dwordx4 a[44:47], v[48:49], off offset:-4096
	s_waitcnt vmcnt(31)
	ds_write_b128 v199, v[14:17] offset:1024
	v_add_co_u32_e32 v14, vcc, s8, v46
	s_movk_i32 s8, 0x4000
	s_nop 0
	v_addc_co_u32_e32 v15, vcc, 0, v47, vcc
	s_waitcnt vmcnt(28)
	ds_write_b128 v199, v[42:45] offset:2048
	v_add_co_u32_e32 v42, vcc, s8, v46
	ds_write_b128 v199, v[34:37]
	s_nop 0
	v_addc_co_u32_e32 v43, vcc, 0, v47, vcc
	s_waitcnt vmcnt(27)
	ds_write_b128 v199, v[38:41] offset:3072
	v_add_co_u32_e32 v44, vcc, s16, v72
	global_load_dwordx4 a[36:39], v[14:15], off offset:1024
	global_load_dwordx4 a[32:35], v[42:43], off offset:1024
	global_load_dwordx4 a[48:51], v[42:43], off offset:2048
	global_load_dwordx4 a[52:55], v[14:15], off offset:2048
	global_load_dwordx4 a[60:63], v[14:15], off offset:3072
	global_load_dwordx4 a[40:43], v[50:51], off offset:-4096
	global_load_dwordx4 v[34:37], v[50:51], off
	global_load_dwordx4 v[38:41], v[48:49], off
	s_nop 0
	global_load_dwordx4 v[14:17], v[48:49], off offset:1024
	s_waitcnt vmcnt(34)
	ds_write_b128 v199, v[52:55] offset:4096
	s_waitcnt vmcnt(33)
	ds_write_b128 v199, v[56:59] offset:5120
	v_addc_co_u32_e32 v45, vcc, 0, v73, vcc
	s_xor_b32 s8, s17, 0x8000
	global_load_dwordx4 a[68:71], v[106:107], off offset:-4096
	s_waitcnt vmcnt(33)
	ds_write_b128 v199, v[60:63] offset:6144
	s_waitcnt vmcnt(32)
	ds_write_b128 v199, v[64:67] offset:7168
	v_add_co_u32_e32 v58, vcc, s16, v110
	s_lshl_b32 s8, s8, 1
	global_load_dwordx4 a[56:59], v[42:43], off offset:3072
	global_load_dwordx4 a[64:67], v[72:73], off
	global_load_dwordx4 a[72:75], v[72:73], off offset:1024
	global_load_dwordx4 a[80:83], v[72:73], off offset:2048
	global_load_dwordx4 a[84:87], v[44:45], off offset:2048
	global_load_dwordx4 a[92:95], v[44:45], off offset:3072
	global_load_dwordx4 a[76:79], v[44:45], off offset:1024
	global_load_dwordx4 a[88:91], v[72:73], off offset:3072
	global_load_dwordx4 v[46:49], v[106:107], off
	global_load_dwordx4 v[54:57], v[106:107], off offset:1024
	s_nop 0
	global_load_dwordx4 v[42:45], v[108:109], off
	global_load_dwordx4 v[50:53], v[108:109], off offset:1024
	s_waitcnt vmcnt(42)
	ds_write_b128 v199, v[68:71] offset:8192
	s_waitcnt vmcnt(41)
	ds_write_b128 v199, v[78:81] offset:9216
	s_waitcnt vmcnt(39)
	ds_write_b128 v199, v[86:89] offset:10240
	ds_write_b128 v199, v[82:85] offset:11264
	v_addc_co_u32_e32 v59, vcc, 0, v111, vcc
	v_lshl_add_u64 v[78:79], v[74:75], 0, s[8:9]
	v_add_co_u32_e32 v84, vcc, s14, v78
	global_load_dwordx4 a[96:99], v[110:111], off
	global_load_dwordx4 a[104:107], v[110:111], off offset:1024
	global_load_dwordx4 a[108:111], v[58:59], off offset:1024
	global_load_dwordx4 a[116:119], v[58:59], off offset:2048
	global_load_dwordx4 a[112:115], v[110:111], off offset:2048
	global_load_dwordx4 a[120:123], v[110:111], off offset:3072
	global_load_dwordx4 a[100:103], v[112:113], off offset:-4096
	global_load_dwordx4 v[62:65], v[112:113], off
	global_load_dwordx4 a[124:127], v[58:59], off offset:3072
	s_nop 0
	global_load_dwordx4 v[58:61], v[114:115], off
	v_addc_co_u32_e32 v85, vcc, 0, v79, vcc
	v_add_co_u32_e32 v82, vcc, s15, v78
	s_add_i32 s8, s11, 0xa000
	s_nop 0
	v_addc_co_u32_e32 v83, vcc, 0, v79, vcc
	global_load_dwordx4 v[110:113], v[82:83], off offset:2048
	global_load_dwordx4 v[106:109], v[84:85], off offset:2048
	s_waitcnt vmcnt(39)
	ds_write_b128 v199, v[90:93] offset:12288
	s_waitcnt vmcnt(37)
	ds_write_b128 v199, v[94:97] offset:13312
	s_waitcnt vmcnt(36)
	ds_write_b128 v199, v[98:101] offset:14336
	s_waitcnt vmcnt(35)
	ds_write_b128 v199, v[102:105] offset:15360
	global_load_dwordx4 a[128:131], v[78:79], off
	global_load_dwordx4 a[132:135], v[84:85], off offset:-4096
	global_load_dwordx4 a[136:139], v[78:79], off offset:1024
	global_load_dwordx4 a[144:147], v[78:79], off offset:2048
	global_load_dwordx4 v[102:105], v[82:83], off offset:3072
	global_load_dwordx4 v[98:101], v[84:85], off offset:3072
	s_and_b32 s8, s8, 0xe000
	v_add_co_u32_e32 v80, vcc, s16, v78
	s_lshl_b32 s8, s8, 1
	s_nop 0
	v_addc_co_u32_e32 v81, vcc, 0, v79, vcc
	v_lshl_add_u64 v[122:123], v[74:75], 0, s[8:9]
	v_add_co_u32_e32 v124, vcc, s14, v122
	s_add_i32 s8, s11, 0xc000
	s_nop 0
	v_addc_co_u32_e32 v125, vcc, 0, v123, vcc
	v_add_co_u32_e32 v126, vcc, s15, v122
	s_and_b32 s8, s8, 0xc000
	s_nop 0
	v_addc_co_u32_e32 v127, vcc, 0, v123, vcc
	global_load_dwordx4 v[70:73], v[124:125], off offset:1024
	global_load_dwordx4 v[114:117], v[124:125], off offset:2048
	global_load_dwordx4 v[66:69], v[126:127], off offset:1024
	global_load_dwordx4 v[118:121], v[126:127], off offset:2048
	global_load_dwordx4 a[148:151], v[80:81], off offset:2048
	global_load_dwordx4 a[156:159], v[80:81], off offset:3072
	global_load_dwordx4 v[132:135], v[126:127], off offset:3072
	global_load_dwordx4 v[136:139], v[124:125], off offset:3072
	global_load_dwordx4 a[140:143], v[80:81], off offset:1024
	global_load_dwordx4 a[152:155], v[78:79], off offset:3072
	s_nop 0
	global_load_dwordx4 v[78:81], v[84:85], off
	global_load_dwordx4 v[86:89], v[84:85], off offset:1024
	s_lshl_b32 s8, s8, 1
	v_lshl_add_u64 v[164:165], v[74:75], 0, s[8:9]
	v_add_co_u32_e32 v176, vcc, s14, v164
	s_add_i32 s11, s11, 0xe000
	s_nop 0
	v_addc_co_u32_e32 v177, vcc, 0, v165, vcc
	v_add_co_u32_e32 v184, vcc, s15, v164
	s_and_b32 s8, s11, 0xe000
	s_nop 0
	v_addc_co_u32_e32 v185, vcc, 0, v165, vcc
	global_load_dwordx4 v[140:143], v[184:185], off offset:2048
	global_load_dwordx4 v[144:147], v[176:177], off offset:2048
	global_load_dwordx4 v[148:151], v[176:177], off offset:3072
	global_load_dwordx4 v[152:155], v[184:185], off offset:3072
	s_lshl_b32 s8, s8, 1
	v_lshl_add_u64 v[186:187], v[74:75], 0, s[8:9]
	v_add_co_u32_e32 v188, vcc, s14, v186
	v_and_or_b32 v74, v76, 16, v200
	s_nop 0
	v_addc_co_u32_e32 v189, vcc, 0, v187, vcc
	v_add_co_u32_e32 v190, vcc, s15, v186
	v_lshlrev_b32_e32 v129, 2, v74
	s_nop 0
	v_addc_co_u32_e32 v191, vcc, 0, v187, vcc
	global_load_dwordx4 v[94:97], v[188:189], off offset:1024
	global_load_dwordx4 v[156:159], v[188:189], off offset:2048
	global_load_dwordx4 v[90:93], v[190:191], off offset:1024
	global_load_dwordx4 v[160:163], v[190:191], off offset:2048
	global_load_dwordx4 v[172:175], v[188:189], off offset:3072
	global_load_dwordx4 v[180:183], v[190:191], off offset:3072
	s_waitcnt lgkmcnt(0)
	global_load_dword v131, v129, s[6:7]
	global_load_dwordx4 v[74:77], v[82:83], off
	s_nop 0
	global_load_dwordx4 v[82:85], v[82:83], off offset:1024
	s_waitcnt vmcnt(32)
	ds_write_b128 v199, v[110:113] offset:16384
	s_waitcnt vmcnt(31)
	ds_write_b128 v199, v[106:109] offset:17408
	v_lshlrev_b32_e32 v106, 7, v130
	v_or3_b32 v202, v106, v128, v179
	v_lshlrev_b32_e32 v106, 9, v201
	v_or_b32_e32 v107, 32, v129
	v_or3_b32 v106, v106, s10, v202
	global_load_dword v178, v129, s[6:7] offset:128
	global_load_dword v192, v107, s[6:7] offset:128
	global_load_dword v193, v129, s[6:7] offset:32
	v_ashrrev_i32_e32 v107, 31, v106
	v_lshl_add_u64 v[128:129], v[106:107], 2, s[4:5]
	global_load_dword v171, v[128:129], off
	s_waitcnt vmcnt(30)
	ds_write_b128 v199, v[102:105] offset:18432
	s_waitcnt vmcnt(29)
	ds_write_b128 v199, v[98:101] offset:19456
	v_add_co_u32_e32 v98, vcc, s16, v122
	s_mov_b32 s14, 0x45000000
	s_nop 0
	v_addc_co_u32_e32 v99, vcc, 0, v123, vcc
	global_load_dwordx4 a[160:163], v[122:123], off
	global_load_dwordx4 a[168:171], v[122:123], off offset:1024
	global_load_dwordx4 a[172:175], v[98:99], off offset:1024
	global_load_dwordx4 a[180:183], v[98:99], off offset:2048
	global_load_dwordx4 a[176:179], v[122:123], off offset:2048
	global_load_dwordx4 a[184:187], v[122:123], off offset:3072
	global_load_dword v170, v[128:129], off offset:64
	global_load_dwordx4 a[164:167], v[124:125], off offset:-4096
	global_load_dwordx4 v[102:105], v[124:125], off
	global_load_dwordx4 a[188:191], v[98:99], off offset:3072
	s_nop 0
	global_load_dwordx4 v[98:101], v[126:127], off
	s_waitcnt vmcnt(36)
	ds_write_b128 v199, v[118:121] offset:20480
	ds_write_b128 v199, v[114:117] offset:21504
	global_load_dword v169, v[128:129], off offset:128
	v_add_co_u32_e32 v106, vcc, s16, v164
	s_waitcnt vmcnt(34)
	ds_write_b128 v199, v[132:135] offset:22528
	s_waitcnt vmcnt(33)
	ds_write_b128 v199, v[136:139] offset:23552
	v_addc_co_u32_e32 v107, vcc, 0, v165, vcc
	global_load_dwordx4 a[192:195], v[164:165], off
	global_load_dwordx4 a[196:199], v[176:177], off offset:-4096
	global_load_dwordx4 a[200:203], v[164:165], off offset:1024
	global_load_dwordx4 a[208:211], v[164:165], off offset:2048
	global_load_dwordx4 a[212:215], v[106:107], off offset:2048
	global_load_dwordx4 a[220:223], v[106:107], off offset:3072
	global_load_dwordx4 a[204:207], v[106:107], off offset:1024
	global_load_dwordx4 a[216:219], v[164:165], off offset:3072
	global_load_dwordx4 v[110:113], v[176:177], off
	global_load_dwordx4 v[118:121], v[176:177], off offset:1024
	s_nop 0
	global_load_dwordx4 v[106:109], v[184:185], off
	global_load_dwordx4 v[114:117], v[184:185], off offset:1024
	global_load_dword v168, v[128:129], off offset:192
	v_add_co_u32_e32 v122, vcc, s16, v186
	v_and_b32_e32 v133, 32, v0
	s_nop 0
	v_addc_co_u32_e32 v123, vcc, 0, v187, vcc
	s_waitcnt vmcnt(41)
	ds_write_b128 v199, v[140:143] offset:24576
	s_waitcnt vmcnt(40)
	ds_write_b128 v199, v[144:147] offset:25600
	s_waitcnt vmcnt(38)
	ds_write_b128 v199, v[152:155] offset:26624
	ds_write_b128 v199, v[148:151] offset:27648
	global_load_dwordx4 a[224:227], v[186:187], off
	global_load_dwordx4 a[232:235], v[186:187], off offset:1024
	global_load_dwordx4 a[236:239], v[122:123], off offset:1024
	global_load_dwordx4 a[244:247], v[122:123], off offset:2048
	global_load_dwordx4 a[240:243], v[186:187], off offset:2048
	global_load_dwordx4 a[248:251], v[186:187], off offset:3072
	global_load_dwordx4 a[228:231], v[188:189], off offset:-4096
	global_load_dwordx4 v[126:129], v[188:189], off
	global_load_dwordx4 a[252:255], v[122:123], off offset:3072
	s_nop 0
	global_load_dwordx4 v[122:125], v[190:191], off
	v_lshlrev_b32_e32 v132, 2, v201
	v_lshl_or_b32 v130, v130, 6, v133
	v_lshrrev_b32_e32 v139, 1, v0
	v_and_b32_e32 v203, 24, v139
	s_waitcnt vmcnt(44)
	ds_write_b128 v199, v[160:163] offset:28672
	ds_write_b128 v199, v[156:159] offset:29696
	s_waitcnt vmcnt(42)
	ds_write_b128 v199, v[180:183] offset:30720
	ds_write_b128 v199, v[172:175] offset:31744
	s_waitcnt vmcnt(10) lgkmcnt(0)
	v_lshrrev_b32_e32 v222, 2, v131
	v_and_or_b32 v222, v222, 8, v132
	v_mul_u32_u24_e32 v222, 0x110, v222
	v_and_or_b32 v223, v131, 31, v130
	v_add_lshl_u32 v223, v223, v222, 1
	v_or_b32_e32 v204, 0x20000, v223
	v_lshrrev_b32_e32 v222, 2, v178
	v_and_or_b32 v222, v222, 8, v132
	v_mul_u32_u24_e32 v222, 0x110, v222
	v_and_or_b32 v223, v178, 31, v130
	v_add_lshl_u32 v223, v223, v222, 1
	v_or_b32_e32 v205, 0x20000, v223
	v_lshrrev_b32_e32 v222, 2, v193
	v_and_or_b32 v222, v222, 8, v132
	v_mul_u32_u24_e32 v222, 0x110, v222
	v_and_or_b32 v223, v193, 31, v130
	v_add_lshl_u32 v223, v223, v222, 1
	v_or_b32_e32 v206, 0x20000, v223
	v_lshrrev_b32_e32 v222, 2, v192
	v_and_or_b32 v222, v222, 8, v132
	v_mul_u32_u24_e32 v222, 0x110, v222
	v_and_or_b32 v223, v192, 31, v130
	v_add_lshl_u32 v223, v223, v222, 1
	v_or_b32_e32 v207, 0x20000, v223
	s_movk_i32 s43, 0x110
	v_mad_u32_u24 v224, v179, s43, v203
	v_mov_b32_e32 v225, 0x20000
	v_lshl_or_b32 v224, v224, 1, v225
	s_lshl_b32 s43, s3, 1
	s_add_u32 s52, s43, 0
	s_and_b32 s52, s52, 7
	s_lshl_b32 s52, s52, 6
	s_nop 0
	v_add_u32_e32 v208, s52, v224
	s_add_u32 s52, s43, 1
	s_and_b32 s52, s52, 7
	s_lshl_b32 s52, s52, 6
	s_sub_u32 s52, s52, 64
	s_nop 0
	v_add_u32_e32 v209, s52, v224
	s_add_u32 s52, s43, 2
	s_and_b32 s52, s52, 7
	s_lshl_b32 s52, s52, 6
	s_nop 0
	v_add_u32_e32 v211, s52, v224
	s_add_u32 s52, s43, 3
	s_and_b32 s52, s52, 7
	s_lshl_b32 s52, s52, 6
	s_nop 0
	v_add_u32_e32 v212, s52, v224
	s_add_u32 s52, s43, 4
	s_and_b32 s52, s52, 7
	s_lshl_b32 s52, s52, 6
	s_nop 0
	v_add_u32_e32 v213, s52, v224
	s_add_u32 s52, s43, 5
	s_and_b32 s52, s52, 7
	s_lshl_b32 s52, s52, 6
	s_nop 0
	v_add_u32_e32 v214, s52, v224
	s_add_u32 s52, s43, 6
	s_and_b32 s52, s52, 7
	s_lshl_b32 s52, s52, 6
	s_nop 0
	v_add_u32_e32 v215, s52, v224
	s_add_u32 s52, s43, 7
	s_and_b32 s52, s52, 7
	s_lshl_b32 s52, s52, 6
	s_nop 0
	v_add_u32_e32 v216, s52, v224
	v_and_b32_e32 v225, 8, v0
	v_cmp_eq_u32_e32 vcc, 0, v225
	v_mov_b32_e32 v225, 0xeeeeeeee
	s_nop 1
	v_cndmask_b32_e32 v210, v225, v196, vcc
	v_and_b32_e32 v225, 47, v0
	v_cmp_eq_u32_e64 s[4:5], 0, v225
	v_lshlrev_b32_e32 v225, 4, v167
	v_lshlrev_b32_e32 v226, 3, v201
	s_mov_b32 s52, 0x24400
	v_or3_b32 v218, v225, v226, s52
	s_load_dwordx2 s[6:7], s[0:1], 0x18
	s_lshl_b32 s11, s2, 9
	s_mov_b64 s[22:23], 0
	s_mov_b32 s29, 0
	s_mov_b32 s30, 0
	v_mov_b32_e32 v221, 0
	s_mov_b32 s40, 0x3a000000
	s_mov_b32 s41, 0x34800000
	s_mov_b32 s42, 0x45000000
	v_mov_b32_e32 v217, 0x24480
	v_mov_b64_e32 v[230:231], 0
	v_mov_b64_e32 v[232:233], 0
	v_mov_b64_e32 v[234:235], 0
	v_mov_b64_e32 v[236:237], 0
	v_mov_b64_e32 v[238:239], 0
	v_mov_b64_e32 v[240:241], 0
	v_mov_b64_e32 v[242:243], 0
	v_mov_b64_e32 v[244:245], 0
	ds_write_b128 v217, v[230:233]
	v_mov_b32_e32 v178, 0
	v_fma_mixlo_f16 v131, v178, v238, v171
	v_fma_mixlo_f16 v139, v178, v238, v170
	v_fma_mixlo_f16 v147, v178, v238, v169
	v_fma_mixlo_f16 v155, v178, v238, v168
	v_fma_f32 v130, v178, v238, v171
	v_fma_f32 v138, v178, v238, v170
	v_fma_f32 v146, v178, v238, v169
	v_fma_f32 v154, v178, v238, v168
	v_fma_mix_f32 v130, v130, 1.0, -v131 op_sel_hi:[0,0,1]
	v_fma_mix_f32 v138, v138, 1.0, -v139 op_sel_hi:[0,0,1]
	v_fma_mix_f32 v146, v146, 1.0, -v147 op_sel_hi:[0,0,1]
	v_fma_mix_f32 v154, v154, 1.0, -v155 op_sel_hi:[0,0,1]
	v_fma_mixlo_f16 v133, v130, s42, 0
	v_fma_mixlo_f16 v141, v138, s42, 0
	v_fma_mixlo_f16 v149, v146, s42, 0
	v_fma_mixlo_f16 v157, v154, s42, 0
	v_fma_mix_f32 v130, v130, s42, -v133 op_sel_hi:[0,0,1]
	v_fma_mix_f32 v138, v138, s42, -v141 op_sel_hi:[0,0,1]
	v_fma_mix_f32 v146, v146, s42, -v149 op_sel_hi:[0,0,1]
	v_fma_mix_f32 v154, v154, s42, -v157 op_sel_hi:[0,0,1]
	v_fma_mixlo_f16 v132, v130, s42, 0
	v_fma_mixlo_f16 v140, v138, s42, 0
	v_fma_mixlo_f16 v148, v146, s42, 0
	v_fma_mixlo_f16 v156, v154, s42, 0
	ds_write_b16 v204, v131
	ds_write_b16 v205, v139
	ds_write_b16 v206, v147
	ds_write_b16 v207, v155
	ds_write_b16 v204, v133 offset:544
	ds_write_b16 v205, v141 offset:544
	ds_write_b16 v206, v149 offset:544
	ds_write_b16 v207, v157 offset:544
	ds_write_b16 v204, v132 offset:1088
	ds_write_b16 v205, v140 offset:1088
	ds_write_b16 v206, v148 offset:1088
	ds_write_b16 v207, v156 offset:1088
	ds_read_b128 v[180:183], v199 offset:0
	s_waitcnt lgkmcnt(6)
	ds_read_b128 v[184:187], v199 offset:1024
	ds_read_b128 v[188:191], v199 offset:4096
	ds_read_b128 v[192:195], v199 offset:5120
	ds_read_b128 v[222:225], v199 offset:8192
	ds_read_b128 v[226:229], v199 offset:9216
	s_mov_b32 s52, 0x3a83126f
	v_mov_b32_e32 v220, 0x358637bd
	s_waitcnt lgkmcnt(0)
	s_barrier
	ds_read_b128 v[130:133], v208
	ds_read_b128 v[134:137], v209 offset:64
	ds_read_b128 v[138:141], v211
	ds_read_b128 v[142:145], v212
	ds_read_b128 v[146:149], v213
	ds_read_b128 v[150:153], v214
	ds_read_b128 v[154:157], v215
	ds_read_b128 v[158:161], v216
	ds_read_b128 v[248:251], v199 offset:12288
	ds_read_b128 v[252:255], v199 offset:13312
	s_waitcnt lgkmcnt(9)
	v_smfmac_f32_16x16x64_f16 v[230:233], v[130:133], a[16:23], v210
	v_fma_f32 v179, |v171|, s52, v220
	v_fma_f32 v196, |v170|, s52, v220
	v_smfmac_f32_16x16x64_f16 v[234:237], v[130:133], v[180:187], v210
	ds_read_b128 v[180:183], v199 offset:16384
	ds_read_b128 v[184:187], v199 offset:17408
	v_fma_f32 v197, |v169|, s52, v220
	s_waitcnt lgkmcnt(10)
	v_smfmac_f32_16x16x64_f16 v[230:233], v[134:137], a[48:55], v210
	v_fma_f32 v198, |v168|, s52, v220
	v_smfmac_f32_16x16x64_f16 v[234:237], v[134:137], v[188:195], v210
	ds_read_b128 v[188:191], v199 offset:20480
	ds_read_b128 v[192:195], v199 offset:21504
	v_rcp_f32_e32 v179, v179
	s_waitcnt lgkmcnt(11)
	v_smfmac_f32_16x16x64_f16 v[230:233], v[138:141], a[80:87], v210
	v_rcp_f32_e32 v196, v196
	v_smfmac_f32_16x16x64_f16 v[234:237], v[138:141], v[222:229], v210
	ds_read_b128 v[222:225], v199 offset:24576
	ds_read_b128 v[226:229], v199 offset:25600
	v_rcp_f32_e32 v197, v197
	s_waitcnt lgkmcnt(12)
	v_smfmac_f32_16x16x64_f16 v[230:233], v[142:145], a[112:119], v210
	v_rcp_f32_e32 v198, v198
	s_waitcnt lgkmcnt(6)
	v_smfmac_f32_16x16x64_f16 v[234:237], v[142:145], v[248:255], v210
	ds_read_b128 v[248:251], v199 offset:28672
	ds_read_b128 v[252:255], v199 offset:29696
	v_mul_f32_e32 v219, v170, v196
	v_smfmac_f32_16x16x64_f16 v[230:233], v[146:149], a[144:151], v210
	v_mul_f32_e32 v166, v219, v219
	s_waitcnt lgkmcnt(6)
	v_smfmac_f32_16x16x64_f16 v[234:237], v[146:149], v[180:187], v210
	ds_read_b128 v[180:183], v199 offset:2048
	ds_read_b128 v[184:187], v199 offset:3072
	v_mul_f32_e32 v219, v171, v179
	v_smfmac_f32_16x16x64_f16 v[230:233], v[150:153], a[176:183], v210
	v_fmac_f32_e32 v166, v219, v219
	s_waitcnt lgkmcnt(6)
	v_smfmac_f32_16x16x64_f16 v[234:237], v[150:153], v[188:195], v210
	ds_read_b128 v[188:191], v199 offset:6144
	ds_read_b128 v[192:195], v199 offset:7168
	v_mul_f32_e32 v219, v169, v197
	v_smfmac_f32_16x16x64_f16 v[230:233], v[154:157], a[208:215], v210
	v_fmac_f32_e32 v166, v219, v219
	s_waitcnt lgkmcnt(6)
	v_smfmac_f32_16x16x64_f16 v[234:237], v[154:157], v[222:229], v210
	ds_read_b128 v[222:225], v199 offset:10240
	ds_read_b128 v[226:229], v199 offset:11264
	v_mul_f32_e32 v219, v168, v198
	s_waitcnt vmcnt(0)
	v_smfmac_f32_16x16x64_f16 v[230:233], v[158:161], a[240:247], v210
	v_fmac_f32_e32 v166, v219, v219
	s_waitcnt lgkmcnt(6)
	v_smfmac_f32_16x16x64_f16 v[234:237], v[158:161], v[248:255], v210
	ds_read_b128 v[248:251], v199 offset:14336
	ds_read_b128 v[252:255], v199 offset:15360
	v_smfmac_f32_16x16x64_f16 v[238:241], v[130:133], a[24:31], v210
	s_waitcnt lgkmcnt(6)
	v_smfmac_f32_16x16x64_f16 v[242:245], v[130:133], v[180:187], v210
	ds_read_b128 v[180:183], v199 offset:18432
	ds_read_b128 v[184:187], v199 offset:19456
	v_smfmac_f32_16x16x64_f16 v[238:241], v[134:137], a[56:63], v210
	v_fmac_f32_e32 v230, s40, v231
	s_waitcnt lgkmcnt(6)
	v_smfmac_f32_16x16x64_f16 v[242:245], v[134:137], v[188:195], v210
	ds_read_b128 v[188:191], v199 offset:22528
	ds_read_b128 v[192:195], v199 offset:23552
	v_fmac_f32_e32 v234, s40, v235
	v_smfmac_f32_16x16x64_f16 v[238:241], v[138:141], a[88:95], v210
	v_fmac_f32_e32 v230, s41, v232
	s_waitcnt lgkmcnt(6)
	v_smfmac_f32_16x16x64_f16 v[242:245], v[138:141], v[222:229], v210
	ds_read_b128 v[222:225], v199 offset:26624
	ds_read_b128 v[226:229], v199 offset:27648
	v_fmac_f32_e32 v234, s41, v236
	v_smfmac_f32_16x16x64_f16 v[238:241], v[142:145], a[120:127], v210
	s_nop 0
	v_permlane32_swap_b32_e32 v230, v234
	s_waitcnt lgkmcnt(6)
	v_smfmac_f32_16x16x64_f16 v[242:245], v[142:145], v[248:255], v210
	ds_read_b128 v[248:251], v199 offset:30720
	ds_read_b128 v[252:255], v199 offset:31744
	v_add_f32_e32 v175, v230, v234
	v_smfmac_f32_16x16x64_f16 v[238:241], v[146:149], a[152:159], v210
	ds_read_b128 v[230:233], v217
	s_waitcnt lgkmcnt(7)
	v_smfmac_f32_16x16x64_f16 v[242:245], v[146:149], v[180:187], v210
	ds_read_b128 v[234:237], v217
	v_smfmac_f32_16x16x64_f16 v[238:241], v[150:153], a[184:191], v210
	s_waitcnt lgkmcnt(6)
	v_smfmac_f32_16x16x64_f16 v[242:245], v[150:153], v[188:195], v210
	v_smfmac_f32_16x16x64_f16 v[238:241], v[154:157], a[216:223], v210
	s_waitcnt lgkmcnt(4)
	v_smfmac_f32_16x16x64_f16 v[242:245], v[154:157], v[222:229], v210
	v_smfmac_f32_16x16x64_f16 v[238:241], v[158:161], a[248:255], v210
	s_waitcnt lgkmcnt(2)
	v_smfmac_f32_16x16x64_f16 v[242:245], v[158:161], v[248:255], v210
	s_waitcnt lgkmcnt(1)
	v_smfmac_f32_16x16x64_f16 v[230:233], v[130:133], a[0:7], v210
	s_waitcnt lgkmcnt(0)
	v_smfmac_f32_16x16x64_f16 v[234:237], v[130:133], v[18:25], v210
	v_smfmac_f32_16x16x64_f16 v[230:233], v[134:137], a[40:47], v210
	v_fmac_f32_e32 v238, s40, v239
	v_smfmac_f32_16x16x64_f16 v[234:237], v[134:137], v[34:41], v210
	v_fmac_f32_e32 v242, s40, v243
	v_smfmac_f32_16x16x64_f16 v[230:233], v[138:141], a[64:71], v210
	v_fmac_f32_e32 v238, s41, v240
	v_smfmac_f32_16x16x64_f16 v[234:237], v[138:141], v[42:49], v210
	v_fmac_f32_e32 v242, s41, v244
	v_smfmac_f32_16x16x64_f16 v[230:233], v[142:145], a[96:103], v210
	s_nop 0
	v_permlane32_swap_b32_e32 v238, v242
	v_smfmac_f32_16x16x64_f16 v[234:237], v[142:145], v[58:65], v210
	v_add_f32_e32 v174, v238, v242
	v_smfmac_f32_16x16x64_f16 v[230:233], v[146:149], a[128:135], v210
	ds_read_b128 v[238:241], v217
	v_smfmac_f32_16x16x64_f16 v[234:237], v[146:149], v[74:81], v210
	ds_read_b128 v[242:245], v217
	v_smfmac_f32_16x16x64_f16 v[230:233], v[150:153], a[160:167], v210
	v_smfmac_f32_16x16x64_f16 v[234:237], v[150:153], v[98:105], v210
	v_smfmac_f32_16x16x64_f16 v[230:233], v[154:157], a[192:199], v210
	v_smfmac_f32_16x16x64_f16 v[234:237], v[154:157], v[106:113], v210
	v_smfmac_f32_16x16x64_f16 v[230:233], v[158:161], a[224:231], v210
	v_smfmac_f32_16x16x64_f16 v[234:237], v[158:161], v[122:129], v210
	s_waitcnt lgkmcnt(1)
	v_smfmac_f32_16x16x64_f16 v[238:241], v[130:133], a[8:15], v210
	s_waitcnt lgkmcnt(0)
	v_smfmac_f32_16x16x64_f16 v[242:245], v[130:133], v[2:9], v210
	v_smfmac_f32_16x16x64_f16 v[238:241], v[134:137], a[32:39], v210
	v_fmac_f32_e32 v230, s40, v231
	v_smfmac_f32_16x16x64_f16 v[242:245], v[134:137], v[10:17], v210
	v_fmac_f32_e32 v234, s40, v235
	v_smfmac_f32_16x16x64_f16 v[238:241], v[138:141], a[72:79], v210
	v_fmac_f32_e32 v230, s41, v232
	v_smfmac_f32_16x16x64_f16 v[242:245], v[138:141], v[50:57], v210
	v_fmac_f32_e32 v234, s41, v236
	v_smfmac_f32_16x16x64_f16 v[238:241], v[142:145], a[104:111], v210
	s_nop 0
	v_permlane32_swap_b32_e32 v230, v234
	v_smfmac_f32_16x16x64_f16 v[242:245], v[142:145], v[26:33], v210
	v_add_f32_e32 v173, v230, v234
	v_smfmac_f32_16x16x64_f16 v[238:241], v[146:149], a[136:143], v210
	ds_read_b128 v[230:233], v217
	v_smfmac_f32_16x16x64_f16 v[242:245], v[146:149], v[82:89], v210
	ds_read_b128 v[234:237], v217
	v_smfmac_f32_16x16x64_f16 v[238:241], v[150:153], a[168:175], v210
	v_smfmac_f32_16x16x64_f16 v[242:245], v[150:153], v[66:73], v210
	v_smfmac_f32_16x16x64_f16 v[238:241], v[154:157], a[200:207], v210
	v_smfmac_f32_16x16x64_f16 v[242:245], v[154:157], v[114:121], v210
	v_smfmac_f32_16x16x64_f16 v[238:241], v[158:161], a[232:239], v210
	v_smfmac_f32_16x16x64_f16 v[242:245], v[158:161], v[90:97], v210
	s_nop 6
	v_fmac_f32_e32 v238, s40, v239
	v_fmac_f32_e32 v242, s40, v243
	v_fmac_f32_e32 v238, s41, v240
	v_fmac_f32_e32 v242, s41, v244
	s_nop 1
	v_permlane32_swap_b32_e32 v238, v242
	v_add_f32_e32 v172, v238, v242
	ds_read_b128 v[180:183], v199 offset:0
	ds_read_b128 v[184:187], v199 offset:1024
	ds_read_b128 v[188:191], v199 offset:4096
	ds_read_b128 v[192:195], v199 offset:5120
	ds_read_b128 v[222:225], v199 offset:8192
	ds_read_b128 v[226:229], v199 offset:9216
	v_mul_f32_e32 v239, 0x3b000000, v172
	v_mul_f32_e32 v239, v239, v196
	v_mul_f32_e32 v167, v239, v239
	v_mul_f32_e32 v239, 0x3b000000, v173
	v_mul_f32_e32 v239, v239, v179
	v_fmac_f32_e32 v167, v239, v239
	v_mul_f32_e32 v239, 0x3b000000, v175
	v_mul_f32_e32 v239, v239, v197
	v_fmac_f32_e32 v167, v239, v239
	v_mul_f32_e32 v239, 0x3b000000, v174
	v_mul_f32_e32 v239, v239, v198
	v_fmac_f32_e32 v167, v239, v239
	v_mov_b32_e32 v130, v166
	v_mov_b32_e32 v131, v167
	s_nop 0
	v_add_f32_dpp v130, v130, v130 quad_perm:[1,0,3,2] row_mask:0xf bank_mask:0xf bound_ctrl:1
	v_add_f32_dpp v131, v131, v131 quad_perm:[1,0,3,2] row_mask:0xf bank_mask:0xf bound_ctrl:1
	s_nop 0
	v_add_f32_dpp v130, v130, v130 quad_perm:[2,3,0,1] row_mask:0xf bank_mask:0xf bound_ctrl:1
	v_add_f32_dpp v131, v131, v131 quad_perm:[2,3,0,1] row_mask:0xf bank_mask:0xf bound_ctrl:1
	s_nop 0
	v_add_f32_dpp v130, v130, v130 row_half_mirror row_mask:0xf bank_mask:0xf bound_ctrl:1
	v_add_f32_dpp v131, v131, v131 row_half_mirror row_mask:0xf bank_mask:0xf bound_ctrl:1
	s_nop 0
	v_add_f32_dpp v130, v130, v130 row_mirror row_mask:0xf bank_mask:0xf bound_ctrl:1
	v_add_f32_dpp v131, v131, v131 row_mirror row_mask:0xf bank_mask:0xf bound_ctrl:1
	v_mov_b32_e32 v240, v130
	v_mov_b32_e32 v241, v131
	s_nop 0
	v_permlane32_swap_b32_e32 v130, v240
	v_permlane32_swap_b32_e32 v131, v241
	v_add_f32_e32 v130, v130, v240
	v_add_f32_e32 v131, v131, v241
	v_add_u32_e32 v242, 0, v218
	v_lshlrev_b32_e32 v243, 3, v201
	v_or_b32_e32 v243, 0x24400, v243
	s_and_saveexec_b64 s[2:3], s[4:5]
	ds_write_b64 v242, v[130:131]
	s_or_b64 exec, exec, s[2:3]
	s_waitcnt lgkmcnt(0)
	s_barrier
	ds_read_b64 v[134:135], v243 offset:0
	ds_read_b64 v[138:139], v243 offset:16
	ds_read_b64 v[142:143], v243 offset:32
	ds_read_b64 v[146:147], v243 offset:48
	s_waitcnt lgkmcnt(2)
	v_add_f32_e32 v238, v134, v138
	s_waitcnt lgkmcnt(1)
	v_add_f32_e32 v238, v238, v142
	s_waitcnt lgkmcnt(0)
	v_add_f32_e32 v238, v238, v146
	v_add_f32_e32 v239, v135, v139
	v_add_f32_e32 v239, v239, v143
	v_add_f32_e32 v239, v239, v147
	v_mul_f32_e32 v238, 0x3b000000, v238
	v_max_f32_e32 v238, 0xda24260, v238
	v_sqrt_f32_e32 v238, v238
	v_mul_f32_e32 v239, 0x3b000000, v239
	v_max_f32_e32 v239, 0xda24260, v239
	v_sqrt_f32_e32 v239, v239
	s_nop 0
	v_mov_b32_e32 v220, v239
	v_rcp_f32_e32 v240, v239
	v_min_f32_e32 v241, v238, v239
	v_mul_f32_e32 v238, 0x3c23d70a, v238
	v_mul_f32_e32 v238, v238, v240
	s_mov_b32 s52, 0x3727c5ac
	v_cmp_ngt_f32_e32 vcc, s52, v241
	v_mov_b32_e32 v240, 0x358637bd
	s_nop 1
	v_cndmask_b32_e32 v219, v240, v238, vcc
	v_mul_f32_e32 v178, 0x3b000000, v219
	v_fma_mixlo_f16 v131, v178, v173, v171
	v_fma_mixlo_f16 v139, v178, v172, v170
	v_fma_mixlo_f16 v147, v178, v175, v169
	v_fma_mixlo_f16 v155, v178, v174, v168
	v_fma_f32 v130, v178, v173, v171
	v_fma_f32 v138, v178, v172, v170
	v_fma_f32 v146, v178, v175, v169
	v_fma_f32 v154, v178, v174, v168
	v_fma_mix_f32 v130, v130, 1.0, -v131 op_sel_hi:[0,0,1]
	v_fma_mix_f32 v138, v138, 1.0, -v139 op_sel_hi:[0,0,1]
	v_fma_mix_f32 v146, v146, 1.0, -v147 op_sel_hi:[0,0,1]
	v_fma_mix_f32 v154, v154, 1.0, -v155 op_sel_hi:[0,0,1]
	v_fma_mixlo_f16 v133, v130, s42, 0
	v_fma_mixlo_f16 v141, v138, s42, 0
	v_fma_mixlo_f16 v149, v146, s42, 0
	v_fma_mixlo_f16 v157, v154, s42, 0
	v_fma_mix_f32 v130, v130, s42, -v133 op_sel_hi:[0,0,1]
	v_fma_mix_f32 v138, v138, s42, -v141 op_sel_hi:[0,0,1]
	v_fma_mix_f32 v146, v146, s42, -v149 op_sel_hi:[0,0,1]
	v_fma_mix_f32 v154, v154, s42, -v157 op_sel_hi:[0,0,1]
	v_fma_mixlo_f16 v132, v130, s42, 0
	v_fma_mixlo_f16 v140, v138, s42, 0
	v_fma_mixlo_f16 v148, v146, s42, 0
	v_fma_mixlo_f16 v156, v154, s42, 0
	ds_write_b16 v204, v131 offset:8704
	ds_write_b16 v205, v139 offset:8704
	ds_write_b16 v206, v147 offset:8704
	ds_write_b16 v207, v155 offset:8704
	ds_write_b16 v204, v133 offset:9248
	ds_write_b16 v205, v141 offset:9248
	ds_write_b16 v206, v149 offset:9248
	ds_write_b16 v207, v157 offset:9248
	ds_write_b16 v204, v132 offset:9792
	ds_write_b16 v205, v140 offset:9792
	ds_write_b16 v206, v148 offset:9792
	ds_write_b16 v207, v156 offset:9792
	s_waitcnt lgkmcnt(0)
	s_barrier
	ds_read_b128 v[130:133], v208 offset:8704
	ds_read_b128 v[134:137], v209 offset:8768
	ds_read_b128 v[138:141], v211 offset:8704
	ds_read_b128 v[142:145], v212 offset:8704
	ds_read_b128 v[146:149], v213 offset:8704
	ds_read_b128 v[150:153], v214 offset:8704
	ds_read_b128 v[154:157], v215 offset:8704
	ds_read_b128 v[158:161], v216 offset:8704
	ds_read_b128 v[248:251], v199 offset:12288
	ds_read_b128 v[252:255], v199 offset:13312
	s_waitcnt lgkmcnt(9)
	v_smfmac_f32_16x16x64_f16 v[230:233], v[130:133], a[16:23], v210
	ds_read_b128 v[238:241], v217
	v_smfmac_f32_16x16x64_f16 v[234:237], v[130:133], v[180:187], v210
	ds_read_b128 v[180:183], v199 offset:16384
	ds_read_b128 v[184:187], v199 offset:17408
	ds_read_b128 v[242:245], v217
	s_waitcnt lgkmcnt(12)
	v_smfmac_f32_16x16x64_f16 v[230:233], v[134:137], a[48:55], v210
	v_smfmac_f32_16x16x64_f16 v[234:237], v[134:137], v[188:195], v210
	ds_read_b128 v[188:191], v199 offset:20480
	s_waitcnt lgkmcnt(6)
	ds_read_b128 v[192:195], v199 offset:21504
	v_smfmac_f32_16x16x64_f16 v[230:233], v[138:141], a[80:87], v210
	v_smfmac_f32_16x16x64_f16 v[234:237], v[138:141], v[222:229], v210
	ds_read_b128 v[222:225], v199 offset:24576
	ds_read_b128 v[226:229], v199 offset:25600
	v_smfmac_f32_16x16x64_f16 v[230:233], v[142:145], a[112:119], v210
	s_waitcnt lgkmcnt(8)
	v_smfmac_f32_16x16x64_f16 v[234:237], v[142:145], v[248:255], v210
	ds_read_b128 v[248:251], v199 offset:28672
	ds_read_b128 v[252:255], v199 offset:29696
	v_smfmac_f32_16x16x64_f16 v[230:233], v[146:149], a[144:151], v210
	s_waitcnt lgkmcnt(7)
	v_smfmac_f32_16x16x64_f16 v[234:237], v[146:149], v[180:187], v210
	ds_read_b128 v[180:183], v199 offset:2048
	ds_read_b128 v[184:187], v199 offset:3072
	v_smfmac_f32_16x16x64_f16 v[230:233], v[150:153], a[176:183], v210
	s_waitcnt lgkmcnt(6)
	v_smfmac_f32_16x16x64_f16 v[234:237], v[150:153], v[188:195], v210
	ds_read_b128 v[188:191], v199 offset:6144
	ds_read_b128 v[192:195], v199 offset:7168
	v_smfmac_f32_16x16x64_f16 v[230:233], v[154:157], a[208:215], v210
	s_waitcnt lgkmcnt(6)
	v_smfmac_f32_16x16x64_f16 v[234:237], v[154:157], v[222:229], v210
	ds_read_b128 v[222:225], v199 offset:10240
	ds_read_b128 v[226:229], v199 offset:11264
	v_smfmac_f32_16x16x64_f16 v[230:233], v[158:161], a[240:247], v210
	s_waitcnt lgkmcnt(6)
	v_smfmac_f32_16x16x64_f16 v[234:237], v[158:161], v[248:255], v210
	ds_read_b128 v[248:251], v199 offset:14336
	ds_read_b128 v[252:255], v199 offset:15360
	v_smfmac_f32_16x16x64_f16 v[238:241], v[130:133], a[24:31], v210
	s_waitcnt lgkmcnt(6)
	v_smfmac_f32_16x16x64_f16 v[242:245], v[130:133], v[180:187], v210
	ds_read_b128 v[180:183], v199 offset:18432
	ds_read_b128 v[184:187], v199 offset:19456
	v_smfmac_f32_16x16x64_f16 v[238:241], v[134:137], a[56:63], v210
	v_fmac_f32_e32 v230, s40, v231
	s_waitcnt lgkmcnt(6)
	v_smfmac_f32_16x16x64_f16 v[242:245], v[134:137], v[188:195], v210
	ds_read_b128 v[188:191], v199 offset:22528
	ds_read_b128 v[192:195], v199 offset:23552
	v_fmac_f32_e32 v234, s40, v235
	v_smfmac_f32_16x16x64_f16 v[238:241], v[138:141], a[88:95], v210
	v_fmac_f32_e32 v230, s41, v232
	s_waitcnt lgkmcnt(6)
	v_smfmac_f32_16x16x64_f16 v[242:245], v[138:141], v[222:229], v210
	ds_read_b128 v[222:225], v199 offset:26624
	ds_read_b128 v[226:229], v199 offset:27648
	v_fmac_f32_e32 v234, s41, v236
	v_smfmac_f32_16x16x64_f16 v[238:241], v[142:145], a[120:127], v210
	s_nop 0
	v_permlane32_swap_b32_e32 v230, v234
	s_waitcnt lgkmcnt(6)
	v_smfmac_f32_16x16x64_f16 v[242:245], v[142:145], v[248:255], v210
	ds_read_b128 v[248:251], v199 offset:30720
	ds_read_b128 v[252:255], v199 offset:31744
	v_add_f32_e32 v164, v230, v234
	v_smfmac_f32_16x16x64_f16 v[238:241], v[146:149], a[152:159], v210
	ds_read_b128 v[230:233], v217
	s_waitcnt lgkmcnt(7)
	v_smfmac_f32_16x16x64_f16 v[242:245], v[146:149], v[180:187], v210
	ds_read_b128 v[234:237], v217
	v_smfmac_f32_16x16x64_f16 v[238:241], v[150:153], a[184:191], v210
	s_waitcnt lgkmcnt(6)
	v_smfmac_f32_16x16x64_f16 v[242:245], v[150:153], v[188:195], v210
	v_smfmac_f32_16x16x64_f16 v[238:241], v[154:157], a[216:223], v210
	s_waitcnt lgkmcnt(4)
	v_smfmac_f32_16x16x64_f16 v[242:245], v[154:157], v[222:229], v210
	v_smfmac_f32_16x16x64_f16 v[238:241], v[158:161], a[248:255], v210
	s_waitcnt lgkmcnt(2)
	v_smfmac_f32_16x16x64_f16 v[242:245], v[158:161], v[248:255], v210
	s_waitcnt lgkmcnt(1)
	v_smfmac_f32_16x16x64_f16 v[230:233], v[130:133], a[0:7], v210
	s_waitcnt lgkmcnt(0)
	v_smfmac_f32_16x16x64_f16 v[234:237], v[130:133], v[18:25], v210
	v_smfmac_f32_16x16x64_f16 v[230:233], v[134:137], a[40:47], v210
	v_fmac_f32_e32 v238, s40, v239
	v_smfmac_f32_16x16x64_f16 v[234:237], v[134:137], v[34:41], v210
	v_fmac_f32_e32 v242, s40, v243
	v_smfmac_f32_16x16x64_f16 v[230:233], v[138:141], a[64:71], v210
	v_fmac_f32_e32 v238, s41, v240
	v_smfmac_f32_16x16x64_f16 v[234:237], v[138:141], v[42:49], v210
	v_fmac_f32_e32 v242, s41, v244
	v_smfmac_f32_16x16x64_f16 v[230:233], v[142:145], a[96:103], v210
	s_nop 0
	v_permlane32_swap_b32_e32 v238, v242
	v_smfmac_f32_16x16x64_f16 v[234:237], v[142:145], v[58:65], v210
	v_add_f32_e32 v165, v238, v242
	v_smfmac_f32_16x16x64_f16 v[230:233], v[146:149], a[128:135], v210
	ds_read_b128 v[238:241], v217
	v_smfmac_f32_16x16x64_f16 v[234:237], v[146:149], v[74:81], v210
	ds_read_b128 v[242:245], v217
	v_smfmac_f32_16x16x64_f16 v[230:233], v[150:153], a[160:167], v210
	v_smfmac_f32_16x16x64_f16 v[234:237], v[150:153], v[98:105], v210
	v_smfmac_f32_16x16x64_f16 v[230:233], v[154:157], a[192:199], v210
	v_smfmac_f32_16x16x64_f16 v[234:237], v[154:157], v[106:113], v210
	v_smfmac_f32_16x16x64_f16 v[230:233], v[158:161], a[224:231], v210
	v_smfmac_f32_16x16x64_f16 v[234:237], v[158:161], v[122:129], v210
	s_waitcnt lgkmcnt(1)
	v_smfmac_f32_16x16x64_f16 v[238:241], v[130:133], a[8:15], v210
	s_waitcnt lgkmcnt(0)
	v_smfmac_f32_16x16x64_f16 v[242:245], v[130:133], v[2:9], v210
	v_smfmac_f32_16x16x64_f16 v[238:241], v[134:137], a[32:39], v210
	v_fmac_f32_e32 v230, s40, v231
	v_smfmac_f32_16x16x64_f16 v[242:245], v[134:137], v[10:17], v210
	v_fmac_f32_e32 v234, s40, v235
	v_smfmac_f32_16x16x64_f16 v[238:241], v[138:141], a[72:79], v210
	v_fmac_f32_e32 v230, s41, v232
	v_smfmac_f32_16x16x64_f16 v[242:245], v[138:141], v[50:57], v210
	v_fmac_f32_e32 v234, s41, v236
	v_smfmac_f32_16x16x64_f16 v[238:241], v[142:145], a[104:111], v210
	s_nop 0
	v_permlane32_swap_b32_e32 v230, v234
	v_smfmac_f32_16x16x64_f16 v[242:245], v[142:145], v[26:33], v210
	v_add_f32_e32 v162, v230, v234
	v_smfmac_f32_16x16x64_f16 v[238:241], v[146:149], a[136:143], v210
	ds_read_b128 v[230:233], v217
	v_smfmac_f32_16x16x64_f16 v[242:245], v[146:149], v[82:89], v210
	ds_read_b128 v[234:237], v217
	v_smfmac_f32_16x16x64_f16 v[238:241], v[150:153], a[168:175], v210
	v_smfmac_f32_16x16x64_f16 v[242:245], v[150:153], v[66:73], v210
	v_smfmac_f32_16x16x64_f16 v[238:241], v[154:157], a[200:207], v210
	v_smfmac_f32_16x16x64_f16 v[242:245], v[154:157], v[114:121], v210
	v_smfmac_f32_16x16x64_f16 v[238:241], v[158:161], a[232:239], v210
	v_smfmac_f32_16x16x64_f16 v[242:245], v[158:161], v[90:97], v210
	s_nop 6
	v_fmac_f32_e32 v238, s40, v239
	v_fmac_f32_e32 v242, s40, v243
	v_fmac_f32_e32 v238, s41, v240
	v_fmac_f32_e32 v242, s41, v244
	s_nop 1
	v_permlane32_swap_b32_e32 v238, v242
	v_add_f32_e32 v163, v238, v242
	ds_read_b128 v[180:183], v199 offset:0
	ds_read_b128 v[184:187], v199 offset:1024
	ds_read_b128 v[188:191], v199 offset:4096
	ds_read_b128 v[192:195], v199 offset:5120
	ds_read_b128 v[222:225], v199 offset:8192
	ds_read_b128 v[226:229], v199 offset:9216
	v_sub_f32_e32 v238, v163, v172
	v_mul_f32_e32 v238, 0x3b000000, v238
	v_mul_f32_e32 v238, v238, v196
	v_mul_f32_e32 v130, v238, v238
	v_sub_f32_e32 v238, v162, v173
	v_mul_f32_e32 v238, 0x3b000000, v238
	v_mul_f32_e32 v238, v238, v179
	v_fmac_f32_e32 v130, v238, v238
	v_sub_f32_e32 v238, v164, v175
	v_mul_f32_e32 v238, 0x3b000000, v238
	v_mul_f32_e32 v238, v238, v197
	v_fmac_f32_e32 v130, v238, v238
	v_sub_f32_e32 v238, v165, v174
	v_mul_f32_e32 v238, 0x3b000000, v238
	v_mul_f32_e32 v238, v238, v198
	v_fmac_f32_e32 v130, v238, v238
	s_nop 1
	v_add_f32_dpp v130, v130, v130 quad_perm:[1,0,3,2] row_mask:0xf bank_mask:0xf bound_ctrl:1
	s_nop 1
	v_add_f32_dpp v130, v130, v130 quad_perm:[2,3,0,1] row_mask:0xf bank_mask:0xf bound_ctrl:1
	s_nop 1
	v_add_f32_dpp v130, v130, v130 row_half_mirror row_mask:0xf bank_mask:0xf bound_ctrl:1
	s_nop 1
	v_add_f32_dpp v130, v130, v130 row_mirror row_mask:0xf bank_mask:0xf bound_ctrl:1
	v_mov_b32_e32 v240, v130
	s_nop 1
	v_permlane32_swap_b32_e32 v130, v240
	v_add_f32_e32 v130, v130, v240
	v_add_u32_e32 v242, 64, v218
	v_lshlrev_b32_e32 v243, 3, v201
	v_or_b32_e32 v243, 0x24440, v243
	s_and_saveexec_b64 s[2:3], s[4:5]
	ds_write_b32 v242, v130
	s_or_b64 exec, exec, s[2:3]
	s_waitcnt lgkmcnt(0)
	s_barrier
	ds_read2_b32 v[134:135], v243 offset1:4
	ds_read2_b32 v[136:137], v243 offset0:8 offset1:12
	s_waitcnt lgkmcnt(1)
	v_add_f32_e32 v238, v134, v135
	s_waitcnt lgkmcnt(0)
	v_add_f32_e32 v238, v238, v136
	v_add_f32_e32 v238, v238, v137
	v_mul_f32_e32 v238, 0x3b000000, v238
	v_max_f32_e32 v238, 0xda24260, v238
	v_rcp_f32_e32 v240, v219
	v_sqrt_f32_e32 v238, v238
	s_nop 0
	v_mul_f32_e32 v238, v240, v238
	v_max_f32_e32 v241, v220, v238
	v_mul_f32_e32 v242, 0x3a83126f, v219
	v_max_f32_e32 v242, 0x358637bd, v242
	v_max_f32_e32 v243, 0x26901d7d, v241
	v_rcp_f32_e32 v243, v243
	s_nop 0
	v_mul_f32_e32 v243, 0x3c23d70a, v243
	v_log_f32_e32 v243, v243
	s_nop 0
	v_mul_f32_e32 v243, 0x3e4ccccd, v243
	v_exp_f32_e32 v243, v243
	s_mov_b32 s52, 0x26901d7d
	v_cmp_ge_f32_e32 vcc, s52, v241
	s_nop 1
	v_cndmask_b32_e32 v243, v243, v242, vcc
	v_mul_f32_e32 v242, 0x42c80000, v219
	v_min3_f32 v1, v242, v243, 1.0
.Lrk_top:
	v_sub_f32_e32 v238, 1.0, v221
	v_min_f32_e32 v178, v1, v238
	v_cmp_eq_f32_e32 vcc, 0, v178
	v_mul_f32_e32 v178, 0x3b000000, v178
	s_cmp_eq_u64 vcc, exec
	s_cbranch_scc1 .Lrk_exit
	s_cmp_gt_i32 s30, 63
	s_cbranch_scc1 .Lrk_exit
	v_mul_f32_e32 v134, 0x3e4ccccd, v173
	v_mul_f32_e32 v142, 0x3e4ccccd, v172
	v_mul_f32_e32 v150, 0x3e4ccccd, v175
	v_mul_f32_e32 v158, 0x3e4ccccd, v174
	v_fma_mixlo_f16 v131, v178, v134, v171
	v_fma_mixlo_f16 v139, v178, v142, v170
	v_fma_mixlo_f16 v147, v178, v150, v169
	v_fma_mixlo_f16 v155, v178, v158, v168
	v_fma_f32 v130, v178, v134, v171
	v_fma_f32 v138, v178, v142, v170
	v_fma_f32 v146, v178, v150, v169
	v_fma_f32 v154, v178, v158, v168
	v_fma_mix_f32 v130, v130, 1.0, -v131 op_sel_hi:[0,0,1]
	v_fma_mix_f32 v138, v138, 1.0, -v139 op_sel_hi:[0,0,1]
	v_fma_mix_f32 v146, v146, 1.0, -v147 op_sel_hi:[0,0,1]
	v_fma_mix_f32 v154, v154, 1.0, -v155 op_sel_hi:[0,0,1]
	v_fma_mixlo_f16 v133, v130, s42, 0
	v_fma_mixlo_f16 v141, v138, s42, 0
	v_fma_mixlo_f16 v149, v146, s42, 0
	v_fma_mixlo_f16 v157, v154, s42, 0
	v_fma_mix_f32 v130, v130, s42, -v133 op_sel_hi:[0,0,1]
	v_fma_mix_f32 v138, v138, s42, -v141 op_sel_hi:[0,0,1]
	v_fma_mix_f32 v146, v146, s42, -v149 op_sel_hi:[0,0,1]
	v_fma_mix_f32 v154, v154, s42, -v157 op_sel_hi:[0,0,1]
	v_fma_mixlo_f16 v132, v130, s42, 0
	v_fma_mixlo_f16 v140, v138, s42, 0
	v_fma_mixlo_f16 v148, v146, s42, 0
	v_fma_mixlo_f16 v156, v154, s42, 0
	ds_write_b16 v204, v131
	ds_write_b16 v205, v139
	ds_write_b16 v206, v147
	ds_write_b16 v207, v155
	ds_write_b16 v204, v133 offset:544
	ds_write_b16 v205, v141 offset:544
	ds_write_b16 v206, v149 offset:544
	ds_write_b16 v207, v157 offset:544
	ds_write_b16 v204, v132 offset:1088
	ds_write_b16 v205, v140 offset:1088
	ds_write_b16 v206, v148 offset:1088
	ds_write_b16 v207, v156 offset:1088
	s_waitcnt lgkmcnt(0)
	s_barrier
	ds_read_b128 v[130:133], v208
	ds_read_b128 v[134:137], v209 offset:64
	ds_read_b128 v[138:141], v211
	ds_read_b128 v[142:145], v212
	ds_read_b128 v[146:149], v213
	ds_read_b128 v[150:153], v214
	ds_read_b128 v[154:157], v215
	ds_read_b128 v[158:161], v216
	ds_read_b128 v[248:251], v199 offset:12288
	ds_read_b128 v[252:255], v199 offset:13312
	s_waitcnt lgkmcnt(9)
	v_smfmac_f32_16x16x64_f16 v[230:233], v[130:133], a[16:23], v210
	ds_read_b128 v[238:241], v217
	v_smfmac_f32_16x16x64_f16 v[234:237], v[130:133], v[180:187], v210
	ds_read_b128 v[180:183], v199 offset:16384
	ds_read_b128 v[184:187], v199 offset:17408
	ds_read_b128 v[242:245], v217
	s_waitcnt lgkmcnt(12)
	v_smfmac_f32_16x16x64_f16 v[230:233], v[134:137], a[48:55], v210
	v_mul_f32_e32 v166, 0x3d99999a, v173
	v_smfmac_f32_16x16x64_f16 v[234:237], v[134:137], v[188:195], v210
	ds_read_b128 v[188:191], v199 offset:20480
	s_waitcnt lgkmcnt(6)
	ds_read_b128 v[192:195], v199 offset:21504
	v_mul_f32_e32 v167, 0x3d99999a, v172
	v_smfmac_f32_16x16x64_f16 v[230:233], v[138:141], a[80:87], v210
	v_mul_f32_e32 v176, 0x3d99999a, v175
	v_smfmac_f32_16x16x64_f16 v[234:237], v[138:141], v[222:229], v210
	ds_read_b128 v[222:225], v199 offset:24576
	ds_read_b128 v[226:229], v199 offset:25600
	v_mul_f32_e32 v177, 0x3d99999a, v174
	v_smfmac_f32_16x16x64_f16 v[230:233], v[142:145], a[112:119], v210
	s_waitcnt lgkmcnt(8)
	v_smfmac_f32_16x16x64_f16 v[234:237], v[142:145], v[248:255], v210
	ds_read_b128 v[248:251], v199 offset:28672
	ds_read_b128 v[252:255], v199 offset:29696
	v_smfmac_f32_16x16x64_f16 v[230:233], v[146:149], a[144:151], v210
	s_waitcnt lgkmcnt(7)
	v_smfmac_f32_16x16x64_f16 v[234:237], v[146:149], v[180:187], v210
	ds_read_b128 v[180:183], v199 offset:2048
	ds_read_b128 v[184:187], v199 offset:3072
	v_smfmac_f32_16x16x64_f16 v[230:233], v[150:153], a[176:183], v210
	s_waitcnt lgkmcnt(6)
	v_smfmac_f32_16x16x64_f16 v[234:237], v[150:153], v[188:195], v210
	ds_read_b128 v[188:191], v199 offset:6144
	ds_read_b128 v[192:195], v199 offset:7168
	v_smfmac_f32_16x16x64_f16 v[230:233], v[154:157], a[208:215], v210
	s_waitcnt lgkmcnt(6)
	v_smfmac_f32_16x16x64_f16 v[234:237], v[154:157], v[222:229], v210
	ds_read_b128 v[222:225], v199 offset:10240
	ds_read_b128 v[226:229], v199 offset:11264
	v_smfmac_f32_16x16x64_f16 v[230:233], v[158:161], a[240:247], v210
	s_waitcnt lgkmcnt(6)
	v_smfmac_f32_16x16x64_f16 v[234:237], v[158:161], v[248:255], v210
	ds_read_b128 v[248:251], v199 offset:14336
	ds_read_b128 v[252:255], v199 offset:15360
	v_smfmac_f32_16x16x64_f16 v[238:241], v[130:133], a[24:31], v210
	s_waitcnt lgkmcnt(6)
	v_smfmac_f32_16x16x64_f16 v[242:245], v[130:133], v[180:187], v210
	ds_read_b128 v[180:183], v199 offset:18432
	ds_read_b128 v[184:187], v199 offset:19456
	v_smfmac_f32_16x16x64_f16 v[238:241], v[134:137], a[56:63], v210
	v_fmac_f32_e32 v230, s40, v231
	v_fmac_f32_e32 v234, s40, v235
	s_waitcnt lgkmcnt(6)
	v_smfmac_f32_16x16x64_f16 v[242:245], v[134:137], v[188:195], v210
	ds_read_b128 v[188:191], v199 offset:22528
	ds_read_b128 v[192:195], v199 offset:23552
	v_fmac_f32_e32 v230, s41, v232
	v_fmac_f32_e32 v234, s41, v236
	v_smfmac_f32_16x16x64_f16 v[238:241], v[138:141], a[88:95], v210
	s_nop 0
	v_permlane32_swap_b32_e32 v230, v234
	v_add_f32_e32 v164, v230, v234
	s_waitcnt lgkmcnt(6)
	v_smfmac_f32_16x16x64_f16 v[242:245], v[138:141], v[222:229], v210
	ds_read_b128 v[222:225], v199 offset:26624
	ds_read_b128 v[226:229], v199 offset:27648
	v_fmac_f32_e32 v176, 0x3e666666, v164
	v_fma_mixlo_f16 v232, v178, v176, v169
	v_smfmac_f32_16x16x64_f16 v[238:241], v[142:145], a[120:127], v210
	v_fma_f32 v231, v178, v176, v169
	v_fma_mix_f32 v231, v231, 1.0, -v232 op_sel_hi:[0,0,1]
	s_waitcnt lgkmcnt(6)
	v_smfmac_f32_16x16x64_f16 v[242:245], v[142:145], v[248:255], v210
	ds_read_b128 v[248:251], v199 offset:30720
	ds_read_b128 v[252:255], v199 offset:31744
	v_fma_mixlo_f16 v235, v231, s42, 0
	v_smfmac_f32_16x16x64_f16 v[238:241], v[146:149], a[152:159], v210
	v_fma_mix_f32 v231, v231, s42, -v235 op_sel_hi:[0,0,1]
	s_waitcnt lgkmcnt(6)
	v_smfmac_f32_16x16x64_f16 v[242:245], v[146:149], v[180:187], v210
	v_fma_mixlo_f16 v233, v231, s42, 0
	v_smfmac_f32_16x16x64_f16 v[238:241], v[150:153], a[184:191], v210
	ds_write_b16 v206, v232 offset:8704
	s_waitcnt lgkmcnt(5)
	v_smfmac_f32_16x16x64_f16 v[242:245], v[150:153], v[188:195], v210
	ds_write_b16 v206, v235 offset:9248
	v_smfmac_f32_16x16x64_f16 v[238:241], v[154:157], a[216:223], v210
	ds_write_b16 v206, v233 offset:9792
	s_waitcnt lgkmcnt(5)
	v_smfmac_f32_16x16x64_f16 v[242:245], v[154:157], v[222:229], v210
	ds_read_b128 v[230:233], v217
	v_smfmac_f32_16x16x64_f16 v[238:241], v[158:161], a[248:255], v210
	ds_read_b128 v[234:237], v217
	s_waitcnt lgkmcnt(5)
	v_smfmac_f32_16x16x64_f16 v[242:245], v[158:161], v[248:255], v210
	s_waitcnt lgkmcnt(1)
	v_smfmac_f32_16x16x64_f16 v[230:233], v[130:133], a[0:7], v210
	s_waitcnt lgkmcnt(0)
	v_smfmac_f32_16x16x64_f16 v[234:237], v[130:133], v[18:25], v210
	v_smfmac_f32_16x16x64_f16 v[230:233], v[134:137], a[40:47], v210
	v_fmac_f32_e32 v238, s40, v239
	v_fmac_f32_e32 v242, s40, v243
	v_smfmac_f32_16x16x64_f16 v[234:237], v[134:137], v[34:41], v210
	v_fmac_f32_e32 v238, s41, v240
	v_fmac_f32_e32 v242, s41, v244
	v_smfmac_f32_16x16x64_f16 v[230:233], v[138:141], a[64:71], v210
	s_nop 0
	v_permlane32_swap_b32_e32 v238, v242
	v_add_f32_e32 v165, v238, v242
	v_smfmac_f32_16x16x64_f16 v[234:237], v[138:141], v[42:49], v210
	v_fmac_f32_e32 v177, 0x3e666666, v165
	v_fma_mixlo_f16 v240, v178, v177, v168
	v_smfmac_f32_16x16x64_f16 v[230:233], v[142:145], a[96:103], v210
	v_fma_f32 v239, v178, v177, v168
	v_fma_mix_f32 v239, v239, 1.0, -v240 op_sel_hi:[0,0,1]
	v_smfmac_f32_16x16x64_f16 v[234:237], v[142:145], v[58:65], v210
	v_fma_mixlo_f16 v243, v239, s42, 0
	v_smfmac_f32_16x16x64_f16 v[230:233], v[146:149], a[128:135], v210
	v_fma_mix_f32 v239, v239, s42, -v243 op_sel_hi:[0,0,1]
	v_smfmac_f32_16x16x64_f16 v[234:237], v[146:149], v[74:81], v210
	v_fma_mixlo_f16 v241, v239, s42, 0
	v_smfmac_f32_16x16x64_f16 v[230:233], v[150:153], a[160:167], v210
	ds_write_b16 v207, v240 offset:8704
	v_smfmac_f32_16x16x64_f16 v[234:237], v[150:153], v[98:105], v210
	ds_write_b16 v207, v243 offset:9248
	v_smfmac_f32_16x16x64_f16 v[230:233], v[154:157], a[192:199], v210
	ds_write_b16 v207, v241 offset:9792
	v_smfmac_f32_16x16x64_f16 v[234:237], v[154:157], v[106:113], v210
	ds_read_b128 v[238:241], v217
	v_smfmac_f32_16x16x64_f16 v[230:233], v[158:161], a[224:231], v210
	ds_read_b128 v[242:245], v217
	v_smfmac_f32_16x16x64_f16 v[234:237], v[158:161], v[122:129], v210
	s_waitcnt lgkmcnt(1)
	v_smfmac_f32_16x16x64_f16 v[238:241], v[130:133], a[8:15], v210
	s_waitcnt lgkmcnt(0)
	v_smfmac_f32_16x16x64_f16 v[242:245], v[130:133], v[2:9], v210
	v_smfmac_f32_16x16x64_f16 v[238:241], v[134:137], a[32:39], v210
	v_fmac_f32_e32 v230, s40, v231
	v_fmac_f32_e32 v234, s40, v235
	v_smfmac_f32_16x16x64_f16 v[242:245], v[134:137], v[10:17], v210
	v_fmac_f32_e32 v230, s41, v232
	v_fmac_f32_e32 v234, s41, v236
	v_smfmac_f32_16x16x64_f16 v[238:241], v[138:141], a[72:79], v210
	s_nop 0
	v_permlane32_swap_b32_e32 v230, v234
	v_add_f32_e32 v162, v230, v234
	v_smfmac_f32_16x16x64_f16 v[242:245], v[138:141], v[50:57], v210
	v_fmac_f32_e32 v166, 0x3e666666, v162
	v_fma_mixlo_f16 v232, v178, v166, v171
	v_smfmac_f32_16x16x64_f16 v[238:241], v[142:145], a[104:111], v210
	v_fma_f32 v231, v178, v166, v171
	v_fma_mix_f32 v231, v231, 1.0, -v232 op_sel_hi:[0,0,1]
	v_smfmac_f32_16x16x64_f16 v[242:245], v[142:145], v[26:33], v210
	v_fma_mixlo_f16 v235, v231, s42, 0
	v_smfmac_f32_16x16x64_f16 v[238:241], v[146:149], a[136:143], v210
	v_fma_mix_f32 v231, v231, s42, -v235 op_sel_hi:[0,0,1]
	v_smfmac_f32_16x16x64_f16 v[242:245], v[146:149], v[82:89], v210
	v_fma_mixlo_f16 v233, v231, s42, 0
	v_smfmac_f32_16x16x64_f16 v[238:241], v[150:153], a[168:175], v210
	ds_write_b16 v204, v232 offset:8704
	v_smfmac_f32_16x16x64_f16 v[242:245], v[150:153], v[66:73], v210
	ds_write_b16 v204, v235 offset:9248
	v_smfmac_f32_16x16x64_f16 v[238:241], v[154:157], a[200:207], v210
	ds_write_b16 v204, v233 offset:9792
	v_smfmac_f32_16x16x64_f16 v[242:245], v[154:157], v[114:121], v210
	ds_read_b128 v[230:233], v217
	v_smfmac_f32_16x16x64_f16 v[238:241], v[158:161], a[232:239], v210
	ds_read_b128 v[234:237], v217
	v_smfmac_f32_16x16x64_f16 v[242:245], v[158:161], v[90:97], v210
	s_nop 5
	v_fmac_f32_e32 v238, s40, v239
	s_nop 0
	v_fmac_f32_e32 v242, s40, v243
	v_fmac_f32_e32 v238, s41, v240
	v_fmac_f32_e32 v242, s41, v244
	s_nop 1
	v_permlane32_swap_b32_e32 v238, v242
	v_add_f32_e32 v163, v238, v242
	v_fmac_f32_e32 v167, 0x3e666666, v163
	v_fma_mixlo_f16 v240, v178, v167, v170
	v_fma_f32 v239, v178, v167, v170
	v_fma_mix_f32 v239, v239, 1.0, -v240 op_sel_hi:[0,0,1]
	v_fma_mixlo_f16 v243, v239, s42, 0
	v_fma_mix_f32 v239, v239, s42, -v243 op_sel_hi:[0,0,1]
	v_fma_mixlo_f16 v241, v239, s42, 0
	ds_write_b16 v205, v240 offset:8704
	ds_write_b16 v205, v243 offset:9248
	ds_write_b16 v205, v241 offset:9792
	ds_read_b128 v[180:183], v199 offset:0
	ds_read_b128 v[184:187], v199 offset:1024
	ds_read_b128 v[188:191], v199 offset:4096
	ds_read_b128 v[192:195], v199 offset:5120
	ds_read_b128 v[222:225], v199 offset:8192
	s_waitcnt lgkmcnt(6)
	ds_read_b128 v[226:229], v199 offset:9216
	s_waitcnt lgkmcnt(0)
	s_barrier
	ds_read_b128 v[130:133], v208 offset:8704
	ds_read_b128 v[134:137], v209 offset:8768
	ds_read_b128 v[138:141], v211 offset:8704
	ds_read_b128 v[142:145], v212 offset:8704
	ds_read_b128 v[146:149], v213 offset:8704
	ds_read_b128 v[150:153], v214 offset:8704
	ds_read_b128 v[154:157], v215 offset:8704
	ds_read_b128 v[158:161], v216 offset:8704
	ds_read_b128 v[248:251], v199 offset:12288
	ds_read_b128 v[252:255], v199 offset:13312
	s_waitcnt lgkmcnt(9)
	v_smfmac_f32_16x16x64_f16 v[230:233], v[130:133], a[16:23], v210
	ds_read_b128 v[238:241], v217
	v_smfmac_f32_16x16x64_f16 v[234:237], v[130:133], v[180:187], v210
	ds_read_b128 v[180:183], v199 offset:16384
	ds_read_b128 v[184:187], v199 offset:17408
	ds_read_b128 v[242:245], v217
	s_waitcnt lgkmcnt(12)
	v_smfmac_f32_16x16x64_f16 v[230:233], v[134:137], a[48:55], v210
	v_mul_f32_e32 v179, 0x3f7a4fa5, v173
	v_smfmac_f32_16x16x64_f16 v[234:237], v[134:137], v[188:195], v210
	ds_read_b128 v[188:191], v199 offset:20480
	s_waitcnt lgkmcnt(6)
	ds_read_b128 v[192:195], v199 offset:21504
	v_fmac_f32_e32 v179, 0xc06eeeef, v162
	v_smfmac_f32_16x16x64_f16 v[230:233], v[138:141], a[80:87], v210
	v_mul_f32_e32 v196, 0x3f7a4fa5, v172
	v_smfmac_f32_16x16x64_f16 v[234:237], v[138:141], v[222:229], v210
	ds_read_b128 v[222:225], v199 offset:24576
	ds_read_b128 v[226:229], v199 offset:25600
	v_fmac_f32_e32 v196, 0xc06eeeef, v163
	v_smfmac_f32_16x16x64_f16 v[230:233], v[142:145], a[112:119], v210
	v_mul_f32_e32 v197, 0x3f7a4fa5, v175
	s_waitcnt lgkmcnt(8)
	v_smfmac_f32_16x16x64_f16 v[234:237], v[142:145], v[248:255], v210
	ds_read_b128 v[248:251], v199 offset:28672
	ds_read_b128 v[252:255], v199 offset:29696
	v_fmac_f32_e32 v197, 0xc06eeeef, v164
	v_smfmac_f32_16x16x64_f16 v[230:233], v[146:149], a[144:151], v210
	v_mul_f32_e32 v198, 0x3f7a4fa5, v174
	s_waitcnt lgkmcnt(7)
	v_smfmac_f32_16x16x64_f16 v[234:237], v[146:149], v[180:187], v210
	ds_read_b128 v[180:183], v199 offset:2048
	ds_read_b128 v[184:187], v199 offset:3072
	v_fmac_f32_e32 v198, 0xc06eeeef, v165
	v_smfmac_f32_16x16x64_f16 v[230:233], v[150:153], a[176:183], v210
	s_waitcnt lgkmcnt(6)
	v_smfmac_f32_16x16x64_f16 v[234:237], v[150:153], v[188:195], v210
	ds_read_b128 v[188:191], v199 offset:6144
	ds_read_b128 v[192:195], v199 offset:7168
	v_smfmac_f32_16x16x64_f16 v[230:233], v[154:157], a[208:215], v210
	s_waitcnt lgkmcnt(6)
	v_smfmac_f32_16x16x64_f16 v[234:237], v[154:157], v[222:229], v210
	ds_read_b128 v[222:225], v199 offset:10240
	ds_read_b128 v[226:229], v199 offset:11264
	v_smfmac_f32_16x16x64_f16 v[230:233], v[158:161], a[240:247], v210
	s_waitcnt lgkmcnt(6)
	v_smfmac_f32_16x16x64_f16 v[234:237], v[158:161], v[248:255], v210
	ds_read_b128 v[248:251], v199 offset:14336
	ds_read_b128 v[252:255], v199 offset:15360
	v_smfmac_f32_16x16x64_f16 v[238:241], v[130:133], a[24:31], v210
	s_waitcnt lgkmcnt(6)
	v_smfmac_f32_16x16x64_f16 v[242:245], v[130:133], v[180:187], v210
	ds_read_b128 v[180:183], v199 offset:18432
	ds_read_b128 v[184:187], v199 offset:19456
	v_smfmac_f32_16x16x64_f16 v[238:241], v[134:137], a[56:63], v210
	v_fmac_f32_e32 v230, s40, v231
	v_fmac_f32_e32 v234, s40, v235
	s_waitcnt lgkmcnt(6)
	v_smfmac_f32_16x16x64_f16 v[242:245], v[134:137], v[188:195], v210
	ds_read_b128 v[188:191], v199 offset:22528
	ds_read_b128 v[192:195], v199 offset:23552
	v_fmac_f32_e32 v230, s41, v232
	v_fmac_f32_e32 v234, s41, v236
	v_smfmac_f32_16x16x64_f16 v[238:241], v[138:141], a[88:95], v210
	s_nop 0
	v_permlane32_swap_b32_e32 v230, v234
	v_add_f32_e32 v176, v230, v234
	s_waitcnt lgkmcnt(6)
	v_smfmac_f32_16x16x64_f16 v[242:245], v[138:141], v[222:229], v210
	ds_read_b128 v[222:225], v199 offset:26624
	ds_read_b128 v[226:229], v199 offset:27648
	v_fmac_f32_e32 v197, 0x40638e39, v176
	v_fma_mixlo_f16 v232, v178, v197, v169
	v_smfmac_f32_16x16x64_f16 v[238:241], v[142:145], a[120:127], v210
	v_fma_f32 v231, v178, v197, v169
	v_fma_mix_f32 v231, v231, 1.0, -v232 op_sel_hi:[0,0,1]
	s_waitcnt lgkmcnt(6)
	v_smfmac_f32_16x16x64_f16 v[242:245], v[142:145], v[248:255], v210
	ds_read_b128 v[248:251], v199 offset:30720
	ds_read_b128 v[252:255], v199 offset:31744
	v_fma_mixlo_f16 v235, v231, s42, 0
	v_smfmac_f32_16x16x64_f16 v[238:241], v[146:149], a[152:159], v210
	v_fma_mix_f32 v231, v231, s42, -v235 op_sel_hi:[0,0,1]
	s_waitcnt lgkmcnt(6)
	v_smfmac_f32_16x16x64_f16 v[242:245], v[146:149], v[180:187], v210
	v_fma_mixlo_f16 v233, v231, s42, 0
	v_smfmac_f32_16x16x64_f16 v[238:241], v[150:153], a[184:191], v210
	ds_write_b16 v206, v232
	s_waitcnt lgkmcnt(5)
	v_smfmac_f32_16x16x64_f16 v[242:245], v[150:153], v[188:195], v210
	ds_write_b16 v206, v235 offset:544
	v_smfmac_f32_16x16x64_f16 v[238:241], v[154:157], a[216:223], v210
	ds_write_b16 v206, v233 offset:1088
	s_waitcnt lgkmcnt(5)
	v_smfmac_f32_16x16x64_f16 v[242:245], v[154:157], v[222:229], v210
	ds_read_b128 v[230:233], v217
	v_smfmac_f32_16x16x64_f16 v[238:241], v[158:161], a[248:255], v210
	ds_read_b128 v[234:237], v217
	s_waitcnt lgkmcnt(5)
	v_smfmac_f32_16x16x64_f16 v[242:245], v[158:161], v[248:255], v210
	s_waitcnt lgkmcnt(1)
	v_smfmac_f32_16x16x64_f16 v[230:233], v[130:133], a[0:7], v210
	s_waitcnt lgkmcnt(0)
	v_smfmac_f32_16x16x64_f16 v[234:237], v[130:133], v[18:25], v210
	v_smfmac_f32_16x16x64_f16 v[230:233], v[134:137], a[40:47], v210
	v_fmac_f32_e32 v238, s40, v239
	v_fmac_f32_e32 v242, s40, v243
	v_smfmac_f32_16x16x64_f16 v[234:237], v[134:137], v[34:41], v210
	v_fmac_f32_e32 v238, s41, v240
	v_fmac_f32_e32 v242, s41, v244
	v_smfmac_f32_16x16x64_f16 v[230:233], v[138:141], a[64:71], v210
	s_nop 0
	v_permlane32_swap_b32_e32 v238, v242
	v_add_f32_e32 v177, v238, v242
	v_smfmac_f32_16x16x64_f16 v[234:237], v[138:141], v[42:49], v210
	v_fmac_f32_e32 v198, 0x40638e39, v177
	v_fma_mixlo_f16 v240, v178, v198, v168
	v_smfmac_f32_16x16x64_f16 v[230:233], v[142:145], a[96:103], v210
	v_fma_f32 v239, v178, v198, v168
	v_fma_mix_f32 v239, v239, 1.0, -v240 op_sel_hi:[0,0,1]
	v_smfmac_f32_16x16x64_f16 v[234:237], v[142:145], v[58:65], v210
	v_fma_mixlo_f16 v243, v239, s42, 0
	v_smfmac_f32_16x16x64_f16 v[230:233], v[146:149], a[128:135], v210
	v_fma_mix_f32 v239, v239, s42, -v243 op_sel_hi:[0,0,1]
	v_smfmac_f32_16x16x64_f16 v[234:237], v[146:149], v[74:81], v210
	v_fma_mixlo_f16 v241, v239, s42, 0
	v_smfmac_f32_16x16x64_f16 v[230:233], v[150:153], a[160:167], v210
	ds_write_b16 v207, v240
	v_smfmac_f32_16x16x64_f16 v[234:237], v[150:153], v[98:105], v210
	ds_write_b16 v207, v243 offset:544
	v_smfmac_f32_16x16x64_f16 v[230:233], v[154:157], a[192:199], v210
	ds_write_b16 v207, v241 offset:1088
	v_smfmac_f32_16x16x64_f16 v[234:237], v[154:157], v[106:113], v210
	ds_read_b128 v[238:241], v217
	v_smfmac_f32_16x16x64_f16 v[230:233], v[158:161], a[224:231], v210
	ds_read_b128 v[242:245], v217
	v_smfmac_f32_16x16x64_f16 v[234:237], v[158:161], v[122:129], v210
	s_waitcnt lgkmcnt(1)
	v_smfmac_f32_16x16x64_f16 v[238:241], v[130:133], a[8:15], v210
	s_waitcnt lgkmcnt(0)
	v_smfmac_f32_16x16x64_f16 v[242:245], v[130:133], v[2:9], v210
	v_smfmac_f32_16x16x64_f16 v[238:241], v[134:137], a[32:39], v210
	v_fmac_f32_e32 v230, s40, v231
	v_fmac_f32_e32 v234, s40, v235
	v_smfmac_f32_16x16x64_f16 v[242:245], v[134:137], v[10:17], v210
	v_fmac_f32_e32 v230, s41, v232
	v_fmac_f32_e32 v234, s41, v236
	v_smfmac_f32_16x16x64_f16 v[238:241], v[138:141], a[72:79], v210
	s_nop 0
	v_permlane32_swap_b32_e32 v230, v234
	v_add_f32_e32 v166, v230, v234
	v_smfmac_f32_16x16x64_f16 v[242:245], v[138:141], v[50:57], v210
	v_fmac_f32_e32 v179, 0x40638e39, v166
	v_fma_mixlo_f16 v232, v178, v179, v171
	v_smfmac_f32_16x16x64_f16 v[238:241], v[142:145], a[104:111], v210
	v_fma_f32 v231, v178, v179, v171
	v_fma_mix_f32 v231, v231, 1.0, -v232 op_sel_hi:[0,0,1]
	v_smfmac_f32_16x16x64_f16 v[242:245], v[142:145], v[26:33], v210
	v_fma_mixlo_f16 v235, v231, s42, 0
	v_smfmac_f32_16x16x64_f16 v[238:241], v[146:149], a[136:143], v210
	v_fma_mix_f32 v231, v231, s42, -v235 op_sel_hi:[0,0,1]
	v_smfmac_f32_16x16x64_f16 v[242:245], v[146:149], v[82:89], v210
	v_fma_mixlo_f16 v233, v231, s42, 0
	v_smfmac_f32_16x16x64_f16 v[238:241], v[150:153], a[168:175], v210
	ds_write_b16 v204, v232
	v_smfmac_f32_16x16x64_f16 v[242:245], v[150:153], v[66:73], v210
	ds_write_b16 v204, v235 offset:544
	v_smfmac_f32_16x16x64_f16 v[238:241], v[154:157], a[200:207], v210
	ds_write_b16 v204, v233 offset:1088
	v_smfmac_f32_16x16x64_f16 v[242:245], v[154:157], v[114:121], v210
	ds_read_b128 v[230:233], v217
	v_smfmac_f32_16x16x64_f16 v[238:241], v[158:161], a[232:239], v210
	ds_read_b128 v[234:237], v217
	v_smfmac_f32_16x16x64_f16 v[242:245], v[158:161], v[90:97], v210
	s_nop 5
	v_fmac_f32_e32 v238, s40, v239
	s_nop 0
	v_fmac_f32_e32 v242, s40, v243
	v_fmac_f32_e32 v238, s41, v240
	v_fmac_f32_e32 v242, s41, v244
	s_nop 1
	v_permlane32_swap_b32_e32 v238, v242
	v_add_f32_e32 v167, v238, v242
	v_fmac_f32_e32 v196, 0x40638e39, v167
	v_fma_mixlo_f16 v240, v178, v196, v170
	v_fma_f32 v239, v178, v196, v170
	v_fma_mix_f32 v239, v239, 1.0, -v240 op_sel_hi:[0,0,1]
	v_fma_mixlo_f16 v243, v239, s42, 0
	v_fma_mix_f32 v239, v239, s42, -v243 op_sel_hi:[0,0,1]
	v_fma_mixlo_f16 v241, v239, s42, 0
	ds_write_b16 v205, v240
	ds_write_b16 v205, v243 offset:544
	ds_write_b16 v205, v241 offset:1088
	ds_read_b128 v[180:183], v199 offset:0
	ds_read_b128 v[184:187], v199 offset:1024
	ds_read_b128 v[188:191], v199 offset:4096
	ds_read_b128 v[192:195], v199 offset:5120
	ds_read_b128 v[222:225], v199 offset:8192
	s_waitcnt lgkmcnt(6)
	ds_read_b128 v[226:229], v199 offset:9216
	s_waitcnt lgkmcnt(0)
	s_barrier
	ds_read_b128 v[130:133], v208
	ds_read_b128 v[134:137], v209 offset:64
	ds_read_b128 v[138:141], v211
	ds_read_b128 v[142:145], v212
	ds_read_b128 v[146:149], v213
	ds_read_b128 v[150:153], v214
	ds_read_b128 v[154:157], v215
	ds_read_b128 v[158:161], v216
	ds_read_b128 v[248:251], v199 offset:12288
	ds_read_b128 v[252:255], v199 offset:13312
	s_waitcnt lgkmcnt(9)
	v_smfmac_f32_16x16x64_f16 v[230:233], v[130:133], a[16:23], v210
	ds_read_b128 v[238:241], v217
	v_smfmac_f32_16x16x64_f16 v[234:237], v[130:133], v[180:187], v210
	ds_read_b128 v[180:183], v199 offset:16384
	ds_read_b128 v[184:187], v199 offset:17408
	ds_read_b128 v[242:245], v217
	s_waitcnt lgkmcnt(12)
	v_smfmac_f32_16x16x64_f16 v[230:233], v[134:137], a[48:55], v210
	v_mul_f32_e32 v219, 0x403cf760, v173
	v_smfmac_f32_16x16x64_f16 v[234:237], v[134:137], v[188:195], v210
	ds_read_b128 v[188:191], v199 offset:20480
	s_waitcnt lgkmcnt(6)
	ds_read_b128 v[192:195], v199 offset:21504
	v_fmac_f32_e32 v219, 0xc139885f, v162
	v_smfmac_f32_16x16x64_f16 v[230:233], v[138:141], a[80:87], v210
	v_fmac_f32_e32 v219, 0x411d2a92, v166
	v_smfmac_f32_16x16x64_f16 v[234:237], v[138:141], v[222:229], v210
	ds_read_b128 v[222:225], v199 offset:24576
	ds_read_b128 v[226:229], v199 offset:25600
	v_mul_f32_e32 v220, 0x403cf760, v172
	v_smfmac_f32_16x16x64_f16 v[230:233], v[142:145], a[112:119], v210
	v_fmac_f32_e32 v220, 0xc139885f, v163
	s_waitcnt lgkmcnt(8)
	v_smfmac_f32_16x16x64_f16 v[234:237], v[142:145], v[248:255], v210
	ds_read_b128 v[248:251], v199 offset:28672
	ds_read_b128 v[252:255], v199 offset:29696
	v_fmac_f32_e32 v220, 0x411d2a92, v167
	v_smfmac_f32_16x16x64_f16 v[230:233], v[146:149], a[144:151], v210
	v_mul_f32_e32 v246, 0x403cf760, v175
	s_waitcnt lgkmcnt(7)
	v_smfmac_f32_16x16x64_f16 v[234:237], v[146:149], v[180:187], v210
	ds_read_b128 v[180:183], v199 offset:2048
	ds_read_b128 v[184:187], v199 offset:3072
	v_fmac_f32_e32 v246, 0xc139885f, v164
	v_smfmac_f32_16x16x64_f16 v[230:233], v[150:153], a[176:183], v210
	v_fmac_f32_e32 v246, 0x411d2a92, v176
	s_waitcnt lgkmcnt(6)
	v_smfmac_f32_16x16x64_f16 v[234:237], v[150:153], v[188:195], v210
	ds_read_b128 v[188:191], v199 offset:6144
	ds_read_b128 v[192:195], v199 offset:7168
	v_mul_f32_e32 v247, 0x403cf760, v174
	v_smfmac_f32_16x16x64_f16 v[230:233], v[154:157], a[208:215], v210
	v_fmac_f32_e32 v247, 0xc139885f, v165
	s_waitcnt lgkmcnt(6)
	v_smfmac_f32_16x16x64_f16 v[234:237], v[154:157], v[222:229], v210
	ds_read_b128 v[222:225], v199 offset:10240
	ds_read_b128 v[226:229], v199 offset:11264
	v_fmac_f32_e32 v247, 0x411d2a92, v177
	v_smfmac_f32_16x16x64_f16 v[230:233], v[158:161], a[240:247], v210
	s_waitcnt lgkmcnt(6)
	v_smfmac_f32_16x16x64_f16 v[234:237], v[158:161], v[248:255], v210
	ds_read_b128 v[248:251], v199 offset:14336
	ds_read_b128 v[252:255], v199 offset:15360
	v_smfmac_f32_16x16x64_f16 v[238:241], v[130:133], a[24:31], v210
	s_waitcnt lgkmcnt(6)
	v_smfmac_f32_16x16x64_f16 v[242:245], v[130:133], v[180:187], v210
	ds_read_b128 v[180:183], v199 offset:18432
	ds_read_b128 v[184:187], v199 offset:19456
	v_smfmac_f32_16x16x64_f16 v[238:241], v[134:137], a[56:63], v210
	v_fmac_f32_e32 v230, s40, v231
	v_fmac_f32_e32 v234, s40, v235
	s_waitcnt lgkmcnt(6)
	v_smfmac_f32_16x16x64_f16 v[242:245], v[134:137], v[188:195], v210
	ds_read_b128 v[188:191], v199 offset:22528
	ds_read_b128 v[192:195], v199 offset:23552
	v_fmac_f32_e32 v230, s41, v232
	v_fmac_f32_e32 v234, s41, v236
	v_smfmac_f32_16x16x64_f16 v[238:241], v[138:141], a[88:95], v210
	s_nop 0
	v_permlane32_swap_b32_e32 v230, v234
	v_add_f32_e32 v197, v230, v234
	s_waitcnt lgkmcnt(6)
	v_smfmac_f32_16x16x64_f16 v[242:245], v[138:141], v[222:229], v210
	ds_read_b128 v[222:225], v199 offset:26624
	ds_read_b128 v[226:229], v199 offset:27648
	v_fmac_f32_e32 v246, 0xbe94e4f6, v197
	v_fma_mixlo_f16 v232, v178, v246, v169
	v_smfmac_f32_16x16x64_f16 v[238:241], v[142:145], a[120:127], v210
	v_fma_f32 v231, v178, v246, v169
	v_fma_mix_f32 v231, v231, 1.0, -v232 op_sel_hi:[0,0,1]
	s_waitcnt lgkmcnt(6)
	v_smfmac_f32_16x16x64_f16 v[242:245], v[142:145], v[248:255], v210
	ds_read_b128 v[248:251], v199 offset:30720
	ds_read_b128 v[252:255], v199 offset:31744
	v_fma_mixlo_f16 v235, v231, s42, 0
	v_smfmac_f32_16x16x64_f16 v[238:241], v[146:149], a[152:159], v210
	v_fma_mix_f32 v231, v231, s42, -v235 op_sel_hi:[0,0,1]
	s_waitcnt lgkmcnt(6)
	v_smfmac_f32_16x16x64_f16 v[242:245], v[146:149], v[180:187], v210
	v_fma_mixlo_f16 v233, v231, s42, 0
	v_smfmac_f32_16x16x64_f16 v[238:241], v[150:153], a[184:191], v210
	ds_write_b16 v206, v232 offset:8704
	s_waitcnt lgkmcnt(5)
	v_smfmac_f32_16x16x64_f16 v[242:245], v[150:153], v[188:195], v210
	ds_write_b16 v206, v235 offset:9248
	v_smfmac_f32_16x16x64_f16 v[238:241], v[154:157], a[216:223], v210
	ds_write_b16 v206, v233 offset:9792
	s_waitcnt lgkmcnt(5)
	v_smfmac_f32_16x16x64_f16 v[242:245], v[154:157], v[222:229], v210
	ds_read_b128 v[230:233], v217
	v_smfmac_f32_16x16x64_f16 v[238:241], v[158:161], a[248:255], v210
	ds_read_b128 v[234:237], v217
	s_waitcnt lgkmcnt(5)
	v_smfmac_f32_16x16x64_f16 v[242:245], v[158:161], v[248:255], v210
	s_waitcnt lgkmcnt(1)
	v_smfmac_f32_16x16x64_f16 v[230:233], v[130:133], a[0:7], v210
	s_waitcnt lgkmcnt(0)
	v_smfmac_f32_16x16x64_f16 v[234:237], v[130:133], v[18:25], v210
	v_smfmac_f32_16x16x64_f16 v[230:233], v[134:137], a[40:47], v210
	v_fmac_f32_e32 v238, s40, v239
	v_fmac_f32_e32 v242, s40, v243
	v_smfmac_f32_16x16x64_f16 v[234:237], v[134:137], v[34:41], v210
	v_fmac_f32_e32 v238, s41, v240
	v_fmac_f32_e32 v242, s41, v244
	v_smfmac_f32_16x16x64_f16 v[230:233], v[138:141], a[64:71], v210
	s_nop 0
	v_permlane32_swap_b32_e32 v238, v242
	v_add_f32_e32 v198, v238, v242
	v_smfmac_f32_16x16x64_f16 v[234:237], v[138:141], v[42:49], v210
	v_fmac_f32_e32 v247, 0xbe94e4f6, v198
	v_fma_mixlo_f16 v240, v178, v247, v168
	v_smfmac_f32_16x16x64_f16 v[230:233], v[142:145], a[96:103], v210
	v_fma_f32 v239, v178, v247, v168
	v_fma_mix_f32 v239, v239, 1.0, -v240 op_sel_hi:[0,0,1]
	v_smfmac_f32_16x16x64_f16 v[234:237], v[142:145], v[58:65], v210
	v_fma_mixlo_f16 v243, v239, s42, 0
	v_smfmac_f32_16x16x64_f16 v[230:233], v[146:149], a[128:135], v210
	v_fma_mix_f32 v239, v239, s42, -v243 op_sel_hi:[0,0,1]
	v_smfmac_f32_16x16x64_f16 v[234:237], v[146:149], v[74:81], v210
	v_fma_mixlo_f16 v241, v239, s42, 0
	v_smfmac_f32_16x16x64_f16 v[230:233], v[150:153], a[160:167], v210
	ds_write_b16 v207, v240 offset:8704
	v_smfmac_f32_16x16x64_f16 v[234:237], v[150:153], v[98:105], v210
	ds_write_b16 v207, v243 offset:9248
	v_smfmac_f32_16x16x64_f16 v[230:233], v[154:157], a[192:199], v210
	ds_write_b16 v207, v241 offset:9792
	v_smfmac_f32_16x16x64_f16 v[234:237], v[154:157], v[106:113], v210
	ds_read_b128 v[238:241], v217
	v_smfmac_f32_16x16x64_f16 v[230:233], v[158:161], a[224:231], v210
	ds_read_b128 v[242:245], v217
	v_smfmac_f32_16x16x64_f16 v[234:237], v[158:161], v[122:129], v210
	s_waitcnt lgkmcnt(1)
	v_smfmac_f32_16x16x64_f16 v[238:241], v[130:133], a[8:15], v210
	s_waitcnt lgkmcnt(0)
	v_smfmac_f32_16x16x64_f16 v[242:245], v[130:133], v[2:9], v210
	v_smfmac_f32_16x16x64_f16 v[238:241], v[134:137], a[32:39], v210
	v_fmac_f32_e32 v230, s40, v231
	v_fmac_f32_e32 v234, s40, v235
	v_smfmac_f32_16x16x64_f16 v[242:245], v[134:137], v[10:17], v210
	v_fmac_f32_e32 v230, s41, v232
	v_fmac_f32_e32 v234, s41, v236
	v_smfmac_f32_16x16x64_f16 v[238:241], v[138:141], a[72:79], v210
	s_nop 0
	v_permlane32_swap_b32_e32 v230, v234
	v_add_f32_e32 v179, v230, v234
	v_smfmac_f32_16x16x64_f16 v[242:245], v[138:141], v[50:57], v210
	v_fmac_f32_e32 v219, 0xbe94e4f6, v179
	v_fma_mixlo_f16 v232, v178, v219, v171
	v_smfmac_f32_16x16x64_f16 v[238:241], v[142:145], a[104:111], v210
	v_fma_f32 v231, v178, v219, v171
	v_fma_mix_f32 v231, v231, 1.0, -v232 op_sel_hi:[0,0,1]
	v_smfmac_f32_16x16x64_f16 v[242:245], v[142:145], v[26:33], v210
	v_fma_mixlo_f16 v235, v231, s42, 0
	v_smfmac_f32_16x16x64_f16 v[238:241], v[146:149], a[136:143], v210
	v_fma_mix_f32 v231, v231, s42, -v235 op_sel_hi:[0,0,1]
	v_smfmac_f32_16x16x64_f16 v[242:245], v[146:149], v[82:89], v210
	v_fma_mixlo_f16 v233, v231, s42, 0
	v_smfmac_f32_16x16x64_f16 v[238:241], v[150:153], a[168:175], v210
	ds_write_b16 v204, v232 offset:8704
	v_smfmac_f32_16x16x64_f16 v[242:245], v[150:153], v[66:73], v210
	ds_write_b16 v204, v235 offset:9248
	v_smfmac_f32_16x16x64_f16 v[238:241], v[154:157], a[200:207], v210
	ds_write_b16 v204, v233 offset:9792
	v_smfmac_f32_16x16x64_f16 v[242:245], v[154:157], v[114:121], v210
	ds_read_b128 v[230:233], v217
	v_smfmac_f32_16x16x64_f16 v[238:241], v[158:161], a[232:239], v210
	ds_read_b128 v[234:237], v217
	v_smfmac_f32_16x16x64_f16 v[242:245], v[158:161], v[90:97], v210
	s_nop 5
	v_fmac_f32_e32 v238, s40, v239
	s_nop 0
	v_fmac_f32_e32 v242, s40, v243
	v_fmac_f32_e32 v238, s41, v240
	v_fmac_f32_e32 v242, s41, v244
	s_nop 1
	v_permlane32_swap_b32_e32 v238, v242
	v_add_f32_e32 v196, v238, v242
	v_fmac_f32_e32 v220, 0xbe94e4f6, v196
	v_fma_mixlo_f16 v240, v178, v220, v170
	v_fma_f32 v239, v178, v220, v170
	v_fma_mix_f32 v239, v239, 1.0, -v240 op_sel_hi:[0,0,1]
	v_fma_mixlo_f16 v243, v239, s42, 0
	v_fma_mix_f32 v239, v239, s42, -v243 op_sel_hi:[0,0,1]
	v_fma_mixlo_f16 v241, v239, s42, 0
	ds_write_b16 v205, v240 offset:8704
	ds_write_b16 v205, v243 offset:9248
	ds_write_b16 v205, v241 offset:9792
	ds_read_b128 v[180:183], v199 offset:0
	ds_read_b128 v[184:187], v199 offset:1024
	ds_read_b128 v[188:191], v199 offset:4096
	ds_read_b128 v[192:195], v199 offset:5120
	ds_read_b128 v[222:225], v199 offset:8192
	s_waitcnt lgkmcnt(6)
	ds_read_b128 v[226:229], v199 offset:9216
	s_waitcnt lgkmcnt(0)
	s_barrier
	ds_read_b128 v[130:133], v208 offset:8704
	ds_read_b128 v[134:137], v209 offset:8768
	ds_read_b128 v[138:141], v211 offset:8704
	ds_read_b128 v[142:145], v212 offset:8704
	ds_read_b128 v[146:149], v213 offset:8704
	ds_read_b128 v[150:153], v214 offset:8704
	ds_read_b128 v[154:157], v215 offset:8704
	ds_read_b128 v[158:161], v216 offset:8704
	s_waitcnt lgkmcnt(7)
	v_smfmac_f32_16x16x64_f16 v[230:233], v[130:133], a[16:23], v210
	ds_read_b128 v[238:241], v217
	ds_read_b128 v[242:245], v217
	v_smfmac_f32_16x16x64_f16 v[234:237], v[130:133], v[180:187], v210
	ds_read_b128 v[180:183], v199 offset:12288
	ds_read_b128 v[184:187], v199 offset:13312
	v_mul_f32_e32 v248, 0x40362960, v173
	v_fmac_f32_e32 v248, 0xc12c1f08, v162
	s_waitcnt lgkmcnt(10)
	v_smfmac_f32_16x16x64_f16 v[230:233], v[134:137], a[48:55], v210
	v_fmac_f32_e32 v248, 0x410e80b5, v166
	v_fmac_f32_e32 v248, 0x3e8e8ba3, v179
	v_smfmac_f32_16x16x64_f16 v[234:237], v[134:137], v[188:195], v210
	ds_read_b128 v[188:191], v199 offset:16384
	ds_read_b128 v[192:195], v199 offset:17408
	v_mul_f32_e32 v249, 0x40362960, v172
	s_waitcnt lgkmcnt(11)
	v_smfmac_f32_16x16x64_f16 v[230:233], v[138:141], a[80:87], v210
	v_fmac_f32_e32 v249, 0xc12c1f08, v163
	v_smfmac_f32_16x16x64_f16 v[234:237], v[138:141], v[222:229], v210
	ds_read_b128 v[222:225], v199 offset:20480
	ds_read_b128 v[226:229], v199 offset:21504
	v_fmac_f32_e32 v249, 0x410e80b5, v167
	s_waitcnt lgkmcnt(12)
	v_smfmac_f32_16x16x64_f16 v[230:233], v[142:145], a[112:119], v210
	v_fmac_f32_e32 v249, 0x3e8e8ba3, v196
	s_waitcnt lgkmcnt(4)
	v_smfmac_f32_16x16x64_f16 v[234:237], v[142:145], v[180:187], v210
	ds_read_b128 v[180:183], v199 offset:24576
	ds_read_b128 v[184:187], v199 offset:25600
	v_mul_f32_e32 v250, 0x40362960, v175
	v_smfmac_f32_16x16x64_f16 v[230:233], v[146:149], a[144:151], v210
	v_fmac_f32_e32 v250, 0xc12c1f08, v164
	s_waitcnt lgkmcnt(4)
	v_smfmac_f32_16x16x64_f16 v[234:237], v[146:149], v[188:195], v210
	ds_read_b128 v[188:191], v199 offset:28672
	ds_read_b128 v[192:195], v199 offset:29696
	v_fmac_f32_e32 v250, 0x410e80b5, v176
	v_smfmac_f32_16x16x64_f16 v[230:233], v[150:153], a[176:183], v210
	v_fmac_f32_e32 v250, 0x3e8e8ba3, v197
	s_waitcnt lgkmcnt(4)
	v_smfmac_f32_16x16x64_f16 v[234:237], v[150:153], v[222:229], v210
	ds_read_b128 v[222:225], v199 offset:2048
	ds_read_b128 v[226:229], v199 offset:3072
	v_mul_f32_e32 v251, 0x40362960, v174
	v_smfmac_f32_16x16x64_f16 v[230:233], v[154:157], a[208:215], v210
	v_fmac_f32_e32 v251, 0xc12c1f08, v165
	s_waitcnt lgkmcnt(4)
	v_smfmac_f32_16x16x64_f16 v[234:237], v[154:157], v[180:187], v210
	ds_read_b128 v[180:183], v199 offset:6144
	ds_read_b128 v[184:187], v199 offset:7168
	v_fmac_f32_e32 v251, 0x410e80b5, v177
	v_smfmac_f32_16x16x64_f16 v[230:233], v[158:161], a[240:247], v210
	v_fmac_f32_e32 v251, 0x3e8e8ba3, v198
	s_waitcnt lgkmcnt(4)
	v_smfmac_f32_16x16x64_f16 v[234:237], v[158:161], v[188:195], v210
	ds_read_b128 v[188:191], v199 offset:10240
	ds_read_b128 v[192:195], v199 offset:11264
	v_smfmac_f32_16x16x64_f16 v[238:241], v[130:133], a[24:31], v210
	s_waitcnt lgkmcnt(4)
	v_smfmac_f32_16x16x64_f16 v[242:245], v[130:133], v[222:229], v210
	ds_read_b128 v[222:225], v199 offset:14336
	ds_read_b128 v[226:229], v199 offset:15360
	v_smfmac_f32_16x16x64_f16 v[238:241], v[134:137], a[56:63], v210
	v_fmac_f32_e32 v230, s40, v231
	v_fmac_f32_e32 v234, s40, v235
	s_waitcnt lgkmcnt(4)
	v_smfmac_f32_16x16x64_f16 v[242:245], v[134:137], v[180:187], v210
	ds_read_b128 v[180:183], v199 offset:18432
	ds_read_b128 v[184:187], v199 offset:19456
	v_fmac_f32_e32 v230, s41, v232
	v_fmac_f32_e32 v234, s41, v236
	v_smfmac_f32_16x16x64_f16 v[238:241], v[138:141], a[88:95], v210
	s_nop 0
	v_permlane32_swap_b32_e32 v230, v234
	v_add_f32_e32 v246, v230, v234
	s_waitcnt lgkmcnt(4)
	v_smfmac_f32_16x16x64_f16 v[242:245], v[138:141], v[188:195], v210
	ds_read_b128 v[188:191], v199 offset:22528
	ds_read_b128 v[192:195], v199 offset:23552
	v_fmac_f32_e32 v250, 0xbe8c0c4c, v246
	v_fma_mixlo_f16 v232, v178, v250, v169
	v_smfmac_f32_16x16x64_f16 v[238:241], v[142:145], a[120:127], v210
	v_fma_f32 v231, v178, v250, v169
	v_fma_mix_f32 v231, v231, 1.0, -v232 op_sel_hi:[0,0,1]
	s_waitcnt lgkmcnt(4)
	v_smfmac_f32_16x16x64_f16 v[242:245], v[142:145], v[222:229], v210
	ds_read_b128 v[222:225], v199 offset:26624
	ds_read_b128 v[226:229], v199 offset:27648
	v_fma_mixlo_f16 v235, v231, s42, 0
	v_smfmac_f32_16x16x64_f16 v[238:241], v[146:149], a[152:159], v210
	v_fma_mix_f32 v231, v231, s42, -v235 op_sel_hi:[0,0,1]
	s_waitcnt lgkmcnt(4)
	v_smfmac_f32_16x16x64_f16 v[242:245], v[146:149], v[180:187], v210
	ds_read_b128 v[180:183], v199 offset:30720
	ds_read_b128 v[184:187], v199 offset:31744
	v_fma_mixlo_f16 v233, v231, s42, 0
	v_smfmac_f32_16x16x64_f16 v[238:241], v[150:153], a[184:191], v210
	ds_write_b16 v206, v232
	s_waitcnt lgkmcnt(5)
	v_smfmac_f32_16x16x64_f16 v[242:245], v[150:153], v[188:195], v210
	ds_write_b16 v206, v235 offset:544
	v_smfmac_f32_16x16x64_f16 v[238:241], v[154:157], a[216:223], v210
	ds_write_b16 v206, v233 offset:1088
	s_waitcnt lgkmcnt(5)
	v_smfmac_f32_16x16x64_f16 v[242:245], v[154:157], v[222:229], v210
	ds_read_b128 v[230:233], v217
	v_smfmac_f32_16x16x64_f16 v[238:241], v[158:161], a[248:255], v210
	ds_read_b128 v[234:237], v217
	s_waitcnt lgkmcnt(5)
	v_smfmac_f32_16x16x64_f16 v[242:245], v[158:161], v[180:187], v210
	s_waitcnt lgkmcnt(1)
	v_smfmac_f32_16x16x64_f16 v[230:233], v[130:133], a[0:7], v210
	s_waitcnt lgkmcnt(0)
	v_smfmac_f32_16x16x64_f16 v[234:237], v[130:133], v[18:25], v210
	v_smfmac_f32_16x16x64_f16 v[230:233], v[134:137], a[40:47], v210
	v_fmac_f32_e32 v238, s40, v239
	v_fmac_f32_e32 v242, s40, v243
	v_smfmac_f32_16x16x64_f16 v[234:237], v[134:137], v[34:41], v210
	v_fmac_f32_e32 v238, s41, v240
	v_fmac_f32_e32 v242, s41, v244
	v_smfmac_f32_16x16x64_f16 v[230:233], v[138:141], a[64:71], v210
	s_nop 0
	v_permlane32_swap_b32_e32 v238, v242
	v_add_f32_e32 v247, v238, v242
	v_smfmac_f32_16x16x64_f16 v[234:237], v[138:141], v[42:49], v210
	v_fmac_f32_e32 v251, 0xbe8c0c4c, v247
	v_fma_mixlo_f16 v240, v178, v251, v168
	v_smfmac_f32_16x16x64_f16 v[230:233], v[142:145], a[96:103], v210
	v_fma_f32 v239, v178, v251, v168
	v_fma_mix_f32 v239, v239, 1.0, -v240 op_sel_hi:[0,0,1]
	v_smfmac_f32_16x16x64_f16 v[234:237], v[142:145], v[58:65], v210
	v_fma_mixlo_f16 v243, v239, s42, 0
	v_smfmac_f32_16x16x64_f16 v[230:233], v[146:149], a[128:135], v210
	v_fma_mix_f32 v239, v239, s42, -v243 op_sel_hi:[0,0,1]
	v_smfmac_f32_16x16x64_f16 v[234:237], v[146:149], v[74:81], v210
	v_fma_mixlo_f16 v241, v239, s42, 0
	v_smfmac_f32_16x16x64_f16 v[230:233], v[150:153], a[160:167], v210
	ds_write_b16 v207, v240
	v_smfmac_f32_16x16x64_f16 v[234:237], v[150:153], v[98:105], v210
	ds_write_b16 v207, v243 offset:544
	v_smfmac_f32_16x16x64_f16 v[230:233], v[154:157], a[192:199], v210
	ds_write_b16 v207, v241 offset:1088
	v_smfmac_f32_16x16x64_f16 v[234:237], v[154:157], v[106:113], v210
	ds_read_b128 v[238:241], v217
	v_smfmac_f32_16x16x64_f16 v[230:233], v[158:161], a[224:231], v210
	ds_read_b128 v[242:245], v217
	v_smfmac_f32_16x16x64_f16 v[234:237], v[158:161], v[122:129], v210
	s_waitcnt lgkmcnt(1)
	v_smfmac_f32_16x16x64_f16 v[238:241], v[130:133], a[8:15], v210
	s_waitcnt lgkmcnt(0)
	v_smfmac_f32_16x16x64_f16 v[242:245], v[130:133], v[2:9], v210
	v_smfmac_f32_16x16x64_f16 v[238:241], v[134:137], a[32:39], v210
	v_fmac_f32_e32 v230, s40, v231
	v_fmac_f32_e32 v234, s40, v235
	v_smfmac_f32_16x16x64_f16 v[242:245], v[134:137], v[10:17], v210
	v_fmac_f32_e32 v230, s41, v232
	v_fmac_f32_e32 v234, s41, v236
	v_smfmac_f32_16x16x64_f16 v[238:241], v[138:141], a[72:79], v210
	s_nop 0
	v_permlane32_swap_b32_e32 v230, v234
	v_add_f32_e32 v219, v230, v234
	v_smfmac_f32_16x16x64_f16 v[242:245], v[138:141], v[50:57], v210
	v_fmac_f32_e32 v248, 0xbe8c0c4c, v219
	v_fma_mixlo_f16 v232, v178, v248, v171
	v_smfmac_f32_16x16x64_f16 v[238:241], v[142:145], a[104:111], v210
	v_fma_f32 v231, v178, v248, v171
	v_fma_mix_f32 v231, v231, 1.0, -v232 op_sel_hi:[0,0,1]
	v_smfmac_f32_16x16x64_f16 v[242:245], v[142:145], v[26:33], v210
	v_fma_mixlo_f16 v235, v231, s42, 0
	v_smfmac_f32_16x16x64_f16 v[238:241], v[146:149], a[136:143], v210
	v_fma_mix_f32 v231, v231, s42, -v235 op_sel_hi:[0,0,1]
	v_smfmac_f32_16x16x64_f16 v[242:245], v[146:149], v[82:89], v210
	v_fma_mixlo_f16 v233, v231, s42, 0
	v_smfmac_f32_16x16x64_f16 v[238:241], v[150:153], a[168:175], v210
	ds_write_b16 v204, v232
	v_smfmac_f32_16x16x64_f16 v[242:245], v[150:153], v[66:73], v210
	ds_write_b16 v204, v235 offset:544
	v_smfmac_f32_16x16x64_f16 v[238:241], v[154:157], a[200:207], v210
	ds_write_b16 v204, v233 offset:1088
	v_smfmac_f32_16x16x64_f16 v[242:245], v[154:157], v[114:121], v210
	ds_read_b128 v[230:233], v217
	v_smfmac_f32_16x16x64_f16 v[238:241], v[158:161], a[232:239], v210
	ds_read_b128 v[234:237], v217
	v_smfmac_f32_16x16x64_f16 v[242:245], v[158:161], v[90:97], v210
	s_nop 5
	v_fmac_f32_e32 v238, s40, v239
	s_nop 0
	v_fmac_f32_e32 v242, s40, v243
	v_fmac_f32_e32 v238, s41, v240
	v_fmac_f32_e32 v242, s41, v244
	s_nop 1
	v_permlane32_swap_b32_e32 v238, v242
	v_add_f32_e32 v220, v238, v242
	v_fmac_f32_e32 v249, 0xbe8c0c4c, v220
	v_fma_mixlo_f16 v240, v178, v249, v170
	v_fma_f32 v239, v178, v249, v170
	v_fma_mix_f32 v239, v239, 1.0, -v240 op_sel_hi:[0,0,1]
	v_fma_mixlo_f16 v243, v239, s42, 0
	v_fma_mix_f32 v239, v239, s42, -v243 op_sel_hi:[0,0,1]
	v_fma_mixlo_f16 v241, v239, s42, 0
	ds_write_b16 v205, v240
	ds_write_b16 v205, v243 offset:544
	ds_write_b16 v205, v241 offset:1088
	ds_read_b128 v[180:183], v199 offset:0
	ds_read_b128 v[184:187], v199 offset:1024
	ds_read_b128 v[188:191], v199 offset:4096
	ds_read_b128 v[192:195], v199 offset:5120
	ds_read_b128 v[222:225], v199 offset:8192
	s_waitcnt lgkmcnt(6)
	ds_read_b128 v[226:229], v199 offset:9216
	s_waitcnt lgkmcnt(0)
	s_barrier
	ds_read_b128 v[130:133], v208
	ds_read_b128 v[134:137], v209 offset:64
	ds_read_b128 v[138:141], v211
	ds_read_b128 v[142:145], v212
	ds_read_b128 v[146:149], v213
	ds_read_b128 v[150:153], v214
	ds_read_b128 v[154:157], v215
	ds_read_b128 v[158:161], v216
	s_waitcnt lgkmcnt(7)
	v_smfmac_f32_16x16x64_f16 v[230:233], v[130:133], a[16:23], v210
	ds_read_b128 v[238:241], v217
	ds_read_b128 v[242:245], v217
	v_smfmac_f32_16x16x64_f16 v[234:237], v[130:133], v[180:187], v210
	ds_read_b128 v[180:183], v199 offset:12288
	ds_read_b128 v[184:187], v199 offset:13312
	v_mul_f32_e32 v252, 0x3dbaaaab, v173
	v_fmac_f32_e32 v252, 0x3ee6024d, v166
	s_waitcnt lgkmcnt(10)
	v_smfmac_f32_16x16x64_f16 v[230:233], v[134:137], a[48:55], v210
	v_fmac_f32_e32 v252, 0x3f26aaab, v179
	v_fmac_f32_e32 v252, 0xbea50e7e, v219
	v_smfmac_f32_16x16x64_f16 v[234:237], v[134:137], v[188:195], v210
	ds_read_b128 v[188:191], v199 offset:16384
	ds_read_b128 v[192:195], v199 offset:17408
	v_mul_f32_e32 v253, 0x3dbaaaab, v172
	s_waitcnt lgkmcnt(11)
	v_smfmac_f32_16x16x64_f16 v[230:233], v[138:141], a[80:87], v210
	v_fmac_f32_e32 v253, 0x3ee6024d, v167
	v_smfmac_f32_16x16x64_f16 v[234:237], v[138:141], v[222:229], v210
	ds_read_b128 v[222:225], v199 offset:20480
	ds_read_b128 v[226:229], v199 offset:21504
	v_fmac_f32_e32 v253, 0x3f26aaab, v196
	s_waitcnt lgkmcnt(12)
	v_smfmac_f32_16x16x64_f16 v[230:233], v[142:145], a[112:119], v210
	v_fmac_f32_e32 v253, 0xbea50e7e, v220
	s_waitcnt lgkmcnt(4)
	v_smfmac_f32_16x16x64_f16 v[234:237], v[142:145], v[180:187], v210
	ds_read_b128 v[180:183], v199 offset:24576
	ds_read_b128 v[184:187], v199 offset:25600
	v_mul_f32_e32 v254, 0x3dbaaaab, v175
	v_smfmac_f32_16x16x64_f16 v[230:233], v[146:149], a[144:151], v210
	v_fmac_f32_e32 v254, 0x3ee6024d, v176
	s_waitcnt lgkmcnt(4)
	v_smfmac_f32_16x16x64_f16 v[234:237], v[146:149], v[188:195], v210
	ds_read_b128 v[188:191], v199 offset:28672
	ds_read_b128 v[192:195], v199 offset:29696
	v_fmac_f32_e32 v254, 0x3f26aaab, v197
	v_smfmac_f32_16x16x64_f16 v[230:233], v[150:153], a[176:183], v210
	v_fmac_f32_e32 v254, 0xbea50e7e, v246
	s_waitcnt lgkmcnt(4)
	v_smfmac_f32_16x16x64_f16 v[234:237], v[150:153], v[222:229], v210
	ds_read_b128 v[222:225], v199 offset:2048
	ds_read_b128 v[226:229], v199 offset:3072
	v_mul_f32_e32 v255, 0x3dbaaaab, v174
	v_smfmac_f32_16x16x64_f16 v[230:233], v[154:157], a[208:215], v210
	v_fmac_f32_e32 v255, 0x3ee6024d, v177
	s_waitcnt lgkmcnt(4)
	v_smfmac_f32_16x16x64_f16 v[234:237], v[154:157], v[180:187], v210
	ds_read_b128 v[180:183], v199 offset:6144
	ds_read_b128 v[184:187], v199 offset:7168
	v_fmac_f32_e32 v255, 0x3f26aaab, v198
	v_smfmac_f32_16x16x64_f16 v[230:233], v[158:161], a[240:247], v210
	v_fmac_f32_e32 v255, 0xbea50e7e, v247
	s_waitcnt lgkmcnt(4)
	v_smfmac_f32_16x16x64_f16 v[234:237], v[158:161], v[188:195], v210
	ds_read_b128 v[188:191], v199 offset:10240
	ds_read_b128 v[192:195], v199 offset:11264
	v_smfmac_f32_16x16x64_f16 v[238:241], v[130:133], a[24:31], v210
	s_waitcnt lgkmcnt(4)
	v_smfmac_f32_16x16x64_f16 v[242:245], v[130:133], v[222:229], v210
	ds_read_b128 v[222:225], v199 offset:14336
	ds_read_b128 v[226:229], v199 offset:15360
	v_smfmac_f32_16x16x64_f16 v[238:241], v[134:137], a[56:63], v210
	v_fmac_f32_e32 v230, s40, v231
	v_fmac_f32_e32 v234, s40, v235
	s_waitcnt lgkmcnt(4)
	v_smfmac_f32_16x16x64_f16 v[242:245], v[134:137], v[180:187], v210
	ds_read_b128 v[180:183], v199 offset:18432
	ds_read_b128 v[184:187], v199 offset:19456
	v_fmac_f32_e32 v230, s41, v232
	v_fmac_f32_e32 v234, s41, v236
	v_smfmac_f32_16x16x64_f16 v[238:241], v[138:141], a[88:95], v210
	s_nop 0
	v_permlane32_swap_b32_e32 v230, v234
	v_add_f32_e32 v250, v230, v234
	s_waitcnt lgkmcnt(4)
	v_smfmac_f32_16x16x64_f16 v[242:245], v[138:141], v[188:195], v210
	ds_read_b128 v[188:191], v199 offset:22528
	ds_read_b128 v[192:195], v199 offset:23552
	v_fmac_f32_e32 v254, 0x3e061862, v250
	v_mov_b32_e32 v236, v254
	v_smfmac_f32_16x16x64_f16 v[238:241], v[142:145], a[120:127], v210
	v_fma_mixlo_f16 v232, v178, v236, v169
	v_fma_f32 v254, v178, v236, v169
	s_waitcnt lgkmcnt(4)
	v_smfmac_f32_16x16x64_f16 v[242:245], v[142:145], v[222:229], v210
	ds_read_b128 v[222:225], v199 offset:26624
	ds_read_b128 v[226:229], v199 offset:27648
	v_fma_mix_f32 v231, v254, 1.0, -v232 op_sel_hi:[0,0,1]
	v_fma_mixlo_f16 v235, v231, s42, 0
	v_smfmac_f32_16x16x64_f16 v[238:241], v[146:149], a[152:159], v210
	v_fma_mix_f32 v231, v231, s42, -v235 op_sel_hi:[0,0,1]
	s_waitcnt lgkmcnt(4)
	v_smfmac_f32_16x16x64_f16 v[242:245], v[146:149], v[180:187], v210
	ds_read_b128 v[180:183], v199 offset:30720
	ds_read_b128 v[184:187], v199 offset:31744
	v_fma_mixlo_f16 v233, v231, s42, 0
	v_smfmac_f32_16x16x64_f16 v[238:241], v[150:153], a[184:191], v210
	ds_write_b16 v206, v232 offset:8704
	s_waitcnt lgkmcnt(5)
	v_smfmac_f32_16x16x64_f16 v[242:245], v[150:153], v[188:195], v210
	ds_write_b16 v206, v235 offset:9248
	v_smfmac_f32_16x16x64_f16 v[238:241], v[154:157], a[216:223], v210
	ds_write_b16 v206, v233 offset:9792
	s_waitcnt lgkmcnt(5)
	v_smfmac_f32_16x16x64_f16 v[242:245], v[154:157], v[222:229], v210
	ds_read_b128 v[230:233], v217
	v_smfmac_f32_16x16x64_f16 v[238:241], v[158:161], a[248:255], v210
	ds_read_b128 v[234:237], v217
	s_waitcnt lgkmcnt(5)
	v_smfmac_f32_16x16x64_f16 v[242:245], v[158:161], v[180:187], v210
	s_waitcnt lgkmcnt(1)
	v_smfmac_f32_16x16x64_f16 v[230:233], v[130:133], a[0:7], v210
	s_waitcnt lgkmcnt(0)
	v_smfmac_f32_16x16x64_f16 v[234:237], v[130:133], v[18:25], v210
	v_smfmac_f32_16x16x64_f16 v[230:233], v[134:137], a[40:47], v210
	v_fmac_f32_e32 v238, s40, v239
	v_fmac_f32_e32 v242, s40, v243
	v_smfmac_f32_16x16x64_f16 v[234:237], v[134:137], v[34:41], v210
	v_fmac_f32_e32 v238, s41, v240
	v_fmac_f32_e32 v242, s41, v244
	v_smfmac_f32_16x16x64_f16 v[230:233], v[138:141], a[64:71], v210
	s_nop 0
	v_permlane32_swap_b32_e32 v238, v242
	v_add_f32_e32 v251, v238, v242
	v_smfmac_f32_16x16x64_f16 v[234:237], v[138:141], v[42:49], v210
	v_fmac_f32_e32 v255, 0x3e061862, v251
	v_mov_b32_e32 v244, v255
	v_smfmac_f32_16x16x64_f16 v[230:233], v[142:145], a[96:103], v210
	v_fma_mixlo_f16 v240, v178, v244, v168
	v_fma_f32 v255, v178, v244, v168
	v_smfmac_f32_16x16x64_f16 v[234:237], v[142:145], v[58:65], v210
	v_fma_mix_f32 v239, v255, 1.0, -v240 op_sel_hi:[0,0,1]
	v_fma_mixlo_f16 v243, v239, s42, 0
	v_smfmac_f32_16x16x64_f16 v[230:233], v[146:149], a[128:135], v210
	v_fma_mix_f32 v239, v239, s42, -v243 op_sel_hi:[0,0,1]
	v_smfmac_f32_16x16x64_f16 v[234:237], v[146:149], v[74:81], v210
	v_fma_mixlo_f16 v241, v239, s42, 0
	v_smfmac_f32_16x16x64_f16 v[230:233], v[150:153], a[160:167], v210
	ds_write_b16 v207, v240 offset:8704
	v_smfmac_f32_16x16x64_f16 v[234:237], v[150:153], v[98:105], v210
	ds_write_b16 v207, v243 offset:9248
	v_smfmac_f32_16x16x64_f16 v[230:233], v[154:157], a[192:199], v210
	ds_write_b16 v207, v241 offset:9792
	v_smfmac_f32_16x16x64_f16 v[234:237], v[154:157], v[106:113], v210
	ds_read_b128 v[238:241], v217
	v_smfmac_f32_16x16x64_f16 v[230:233], v[158:161], a[224:231], v210
	ds_read_b128 v[242:245], v217
	v_smfmac_f32_16x16x64_f16 v[234:237], v[158:161], v[122:129], v210
	s_waitcnt lgkmcnt(1)
	v_smfmac_f32_16x16x64_f16 v[238:241], v[130:133], a[8:15], v210
	s_waitcnt lgkmcnt(0)
	v_smfmac_f32_16x16x64_f16 v[242:245], v[130:133], v[2:9], v210
	v_smfmac_f32_16x16x64_f16 v[238:241], v[134:137], a[32:39], v210
	v_fmac_f32_e32 v230, s40, v231
	v_fmac_f32_e32 v234, s40, v235
	v_smfmac_f32_16x16x64_f16 v[242:245], v[134:137], v[10:17], v210
	v_fmac_f32_e32 v230, s41, v232
	v_fmac_f32_e32 v234, s41, v236
	v_smfmac_f32_16x16x64_f16 v[238:241], v[138:141], a[72:79], v210
	s_nop 0
	v_permlane32_swap_b32_e32 v230, v234
	v_add_f32_e32 v248, v230, v234
	v_smfmac_f32_16x16x64_f16 v[242:245], v[138:141], v[50:57], v210
	v_fmac_f32_e32 v252, 0x3e061862, v248
	v_mov_b32_e32 v236, v252
	v_smfmac_f32_16x16x64_f16 v[238:241], v[142:145], a[104:111], v210
	v_fma_mixlo_f16 v232, v178, v236, v171
	v_fma_f32 v252, v178, v236, v171
	v_smfmac_f32_16x16x64_f16 v[242:245], v[142:145], v[26:33], v210
	v_fma_mix_f32 v231, v252, 1.0, -v232 op_sel_hi:[0,0,1]
	v_fma_mixlo_f16 v235, v231, s42, 0
	v_smfmac_f32_16x16x64_f16 v[238:241], v[146:149], a[136:143], v210
	v_fma_mix_f32 v231, v231, s42, -v235 op_sel_hi:[0,0,1]
	v_smfmac_f32_16x16x64_f16 v[242:245], v[146:149], v[82:89], v210
	v_fma_mixlo_f16 v233, v231, s42, 0
	v_smfmac_f32_16x16x64_f16 v[238:241], v[150:153], a[168:175], v210
	ds_write_b16 v204, v232 offset:8704
	v_smfmac_f32_16x16x64_f16 v[242:245], v[150:153], v[66:73], v210
	ds_write_b16 v204, v235 offset:9248
	v_smfmac_f32_16x16x64_f16 v[238:241], v[154:157], a[200:207], v210
	ds_write_b16 v204, v233 offset:9792
	v_smfmac_f32_16x16x64_f16 v[242:245], v[154:157], v[114:121], v210
	ds_read_b128 v[230:233], v217
	v_smfmac_f32_16x16x64_f16 v[238:241], v[158:161], a[232:239], v210
	ds_read_b128 v[234:237], v217
	v_smfmac_f32_16x16x64_f16 v[242:245], v[158:161], v[90:97], v210
	s_nop 5
	v_fmac_f32_e32 v238, s40, v239
	s_nop 0
	v_fmac_f32_e32 v242, s40, v243
	v_fmac_f32_e32 v238, s41, v240
	v_fmac_f32_e32 v242, s41, v244
	s_nop 1
	v_permlane32_swap_b32_e32 v238, v242
	v_add_f32_e32 v249, v238, v242
	v_fmac_f32_e32 v253, 0x3e061862, v249
	v_mov_b32_e32 v244, v253
	v_fma_mixlo_f16 v240, v178, v244, v170
	v_fma_f32 v253, v178, v244, v170
	v_fma_mix_f32 v239, v253, 1.0, -v240 op_sel_hi:[0,0,1]
	v_fma_mixlo_f16 v243, v239, s42, 0
	v_fma_mix_f32 v239, v239, s42, -v243 op_sel_hi:[0,0,1]
	v_fma_mixlo_f16 v241, v239, s42, 0
	ds_write_b16 v205, v240 offset:8704
	ds_write_b16 v205, v243 offset:9248
	ds_write_b16 v205, v241 offset:9792
	ds_read_b128 v[180:183], v199 offset:0
	ds_read_b128 v[184:187], v199 offset:1024
	ds_read_b128 v[188:191], v199 offset:4096
	ds_read_b128 v[192:195], v199 offset:5120
	ds_read_b128 v[222:225], v199 offset:8192
	s_waitcnt lgkmcnt(6)
	ds_read_b128 v[226:229], v199 offset:9216
	s_waitcnt lgkmcnt(0)
	s_barrier
	ds_read_b128 v[130:133], v208 offset:8704
	ds_read_b128 v[134:137], v209 offset:8768
	ds_read_b128 v[138:141], v211 offset:8704
	ds_read_b128 v[142:145], v212 offset:8704
	ds_read_b128 v[146:149], v213 offset:8704
	ds_read_b128 v[150:153], v214 offset:8704
	ds_read_b128 v[154:157], v215 offset:8704
	ds_read_b128 v[158:161], v216 offset:8704
	s_waitcnt lgkmcnt(7)
	v_smfmac_f32_16x16x64_f16 v[230:233], v[130:133], a[16:23], v210
	ds_read_b128 v[238:241], v217
	ds_read_b128 v[242:245], v217
	v_smfmac_f32_16x16x64_f16 v[234:237], v[130:133], v[180:187], v210
	ds_read_b128 v[180:183], v199 offset:12288
	ds_read_b128 v[184:187], v199 offset:13312
	v_mul_f32_e32 v162, 0x3aa1907f, v173
	v_fmac_f32_e32 v162, 0xbb8b5ad3, v166
	s_waitcnt lgkmcnt(10)
	v_smfmac_f32_16x16x64_f16 v[230:233], v[134:137], a[48:55], v210
	v_fmac_f32_e32 v162, 0x3d177777, v179
	v_fmac_f32_e32 v162, 0xbd50568f, v219
	v_smfmac_f32_16x16x64_f16 v[234:237], v[134:137], v[188:195], v210
	ds_read_b128 v[188:191], v199 offset:16384
	ds_read_b128 v[192:195], v199 offset:17408
	v_fmac_f32_e32 v162, 0x3d2ba454, v248
	v_mul_f32_e32 v163, 0x3aa1907f, v172
	s_waitcnt lgkmcnt(11)
	v_smfmac_f32_16x16x64_f16 v[230:233], v[138:141], a[80:87], v210
	v_fmac_f32_e32 v163, 0xbb8b5ad3, v167
	v_fmac_f32_e32 v163, 0x3d177777, v196
	v_smfmac_f32_16x16x64_f16 v[234:237], v[138:141], v[222:229], v210
	ds_read_b128 v[222:225], v199 offset:20480
	ds_read_b128 v[226:229], v199 offset:21504
	v_fmac_f32_e32 v163, 0xbd50568f, v220
	v_fmac_f32_e32 v163, 0x3d2ba454, v249
	s_waitcnt lgkmcnt(12)
	v_smfmac_f32_16x16x64_f16 v[230:233], v[142:145], a[112:119], v210
	v_mul_f32_e32 v164, 0x3aa1907f, v175
	v_fmac_f32_e32 v164, 0xbb8b5ad3, v176
	s_waitcnt lgkmcnt(4)
	v_smfmac_f32_16x16x64_f16 v[234:237], v[142:145], v[180:187], v210
	ds_read_b128 v[180:183], v199 offset:24576
	ds_read_b128 v[184:187], v199 offset:25600
	v_fmac_f32_e32 v164, 0x3d177777, v197
	v_fmac_f32_e32 v164, 0xbd50568f, v246
	v_smfmac_f32_16x16x64_f16 v[230:233], v[146:149], a[144:151], v210
	v_fmac_f32_e32 v164, 0x3d2ba454, v250
	v_mul_f32_e32 v165, 0x3aa1907f, v174
	s_waitcnt lgkmcnt(4)
	v_smfmac_f32_16x16x64_f16 v[234:237], v[146:149], v[188:195], v210
	ds_read_b128 v[188:191], v199 offset:28672
	ds_read_b128 v[192:195], v199 offset:29696
	v_fmac_f32_e32 v165, 0xbb8b5ad3, v177
	v_fmac_f32_e32 v165, 0x3d177777, v198
	v_smfmac_f32_16x16x64_f16 v[230:233], v[150:153], a[176:183], v210
	v_fmac_f32_e32 v165, 0xbd50568f, v247
	v_fmac_f32_e32 v165, 0x3d2ba454, v251
	s_waitcnt lgkmcnt(4)
	v_smfmac_f32_16x16x64_f16 v[234:237], v[150:153], v[222:229], v210
	ds_read_b128 v[222:225], v199 offset:2048
	ds_read_b128 v[226:229], v199 offset:3072
	v_max_f32_e64 v179, |v171|, |v252|
	v_mov_b32_e32 v248, 0x358637bd
	v_smfmac_f32_16x16x64_f16 v[230:233], v[154:157], a[208:215], v210
	v_fmac_f32_e32 v248, 0x3a83126f, v179
	v_rcp_f32_e32 v179, v248
	s_waitcnt lgkmcnt(4)
	v_smfmac_f32_16x16x64_f16 v[234:237], v[154:157], v[180:187], v210
	ds_read_b128 v[180:183], v199 offset:6144
	ds_read_b128 v[184:187], v199 offset:7168
	v_max_f32_e64 v196, |v170|, |v253|
	v_mov_b32_e32 v249, 0x358637bd
	v_smfmac_f32_16x16x64_f16 v[230:233], v[158:161], a[240:247], v210
	v_fmac_f32_e32 v249, 0x3a83126f, v196
	v_rcp_f32_e32 v196, v249
	s_waitcnt lgkmcnt(4)
	v_smfmac_f32_16x16x64_f16 v[234:237], v[158:161], v[188:195], v210
	ds_read_b128 v[188:191], v199 offset:10240
	ds_read_b128 v[192:195], v199 offset:11264
	v_max_f32_e64 v197, |v169|, |v254|
	v_mov_b32_e32 v250, 0x358637bd
	v_fmac_f32_e32 v250, 0x3a83126f, v197
	v_rcp_f32_e32 v197, v250
	v_max_f32_e64 v198, |v168|, |v255|
	v_mov_b32_e32 v251, 0x358637bd
	v_fmac_f32_e32 v251, 0x3a83126f, v198
	v_rcp_f32_e32 v198, v251
	v_smfmac_f32_16x16x64_f16 v[238:241], v[130:133], a[24:31], v210
	s_waitcnt lgkmcnt(4)
	v_smfmac_f32_16x16x64_f16 v[242:245], v[130:133], v[222:229], v210
	ds_read_b128 v[222:225], v199 offset:14336
	ds_read_b128 v[226:229], v199 offset:15360
	v_smfmac_f32_16x16x64_f16 v[238:241], v[134:137], a[56:63], v210
	v_fmac_f32_e32 v230, s40, v231
	s_waitcnt lgkmcnt(4)
	v_smfmac_f32_16x16x64_f16 v[242:245], v[134:137], v[180:187], v210
	ds_read_b128 v[180:183], v199 offset:18432
	ds_read_b128 v[184:187], v199 offset:19456
	v_fmac_f32_e32 v234, s40, v235
	v_smfmac_f32_16x16x64_f16 v[238:241], v[138:141], a[88:95], v210
	v_fmac_f32_e32 v230, s41, v232
	s_waitcnt lgkmcnt(4)
	v_smfmac_f32_16x16x64_f16 v[242:245], v[138:141], v[188:195], v210
	ds_read_b128 v[188:191], v199 offset:22528
	ds_read_b128 v[192:195], v199 offset:23552
	v_fmac_f32_e32 v234, s41, v236
	v_smfmac_f32_16x16x64_f16 v[238:241], v[142:145], a[120:127], v210
	s_nop 0
	v_permlane32_swap_b32_e32 v230, v234
	s_waitcnt lgkmcnt(4)
	v_smfmac_f32_16x16x64_f16 v[242:245], v[142:145], v[222:229], v210
	ds_read_b128 v[222:225], v199 offset:26624
	ds_read_b128 v[226:229], v199 offset:27648
	v_add_f32_e32 v176, v230, v234
	v_smfmac_f32_16x16x64_f16 v[238:241], v[146:149], a[152:159], v210
	v_fmac_f32_e32 v164, 0xbccccccd, v176
	s_waitcnt lgkmcnt(4)
	v_smfmac_f32_16x16x64_f16 v[242:245], v[146:149], v[180:187], v210
	ds_read_b128 v[180:183], v199 offset:30720
	ds_read_b128 v[184:187], v199 offset:31744
	v_mul_f32_e32 v231, v178, v164
	v_smfmac_f32_16x16x64_f16 v[238:241], v[150:153], a[184:191], v210
	v_mul_f32_e32 v231, v231, v197
	s_waitcnt lgkmcnt(4)
	v_smfmac_f32_16x16x64_f16 v[242:245], v[150:153], v[188:195], v210
	v_mul_f32_e32 v219, v231, v231
	v_smfmac_f32_16x16x64_f16 v[238:241], v[154:157], a[216:223], v210
	ds_read_b128 v[230:233], v217
	s_waitcnt lgkmcnt(3)
	v_smfmac_f32_16x16x64_f16 v[242:245], v[154:157], v[222:229], v210
	ds_read_b128 v[234:237], v217
	v_smfmac_f32_16x16x64_f16 v[238:241], v[158:161], a[248:255], v210
	s_waitcnt lgkmcnt(2)
	v_smfmac_f32_16x16x64_f16 v[242:245], v[158:161], v[180:187], v210
	s_waitcnt lgkmcnt(1)
	v_smfmac_f32_16x16x64_f16 v[230:233], v[130:133], a[0:7], v210
	s_waitcnt lgkmcnt(0)
	v_smfmac_f32_16x16x64_f16 v[234:237], v[130:133], v[18:25], v210
	v_smfmac_f32_16x16x64_f16 v[230:233], v[134:137], a[40:47], v210
	v_fmac_f32_e32 v238, s40, v239
	v_smfmac_f32_16x16x64_f16 v[234:237], v[134:137], v[34:41], v210
	v_fmac_f32_e32 v242, s40, v243
	v_smfmac_f32_16x16x64_f16 v[230:233], v[138:141], a[64:71], v210
	v_fmac_f32_e32 v238, s41, v240
	v_smfmac_f32_16x16x64_f16 v[234:237], v[138:141], v[42:49], v210
	v_fmac_f32_e32 v242, s41, v244
	v_smfmac_f32_16x16x64_f16 v[230:233], v[142:145], a[96:103], v210
	s_nop 0
	v_permlane32_swap_b32_e32 v238, v242
	v_smfmac_f32_16x16x64_f16 v[234:237], v[142:145], v[58:65], v210
	v_add_f32_e32 v177, v238, v242
	v_smfmac_f32_16x16x64_f16 v[230:233], v[146:149], a[128:135], v210
	v_fmac_f32_e32 v165, 0xbccccccd, v177
	v_smfmac_f32_16x16x64_f16 v[234:237], v[146:149], v[74:81], v210
	v_mul_f32_e32 v239, v178, v165
	v_smfmac_f32_16x16x64_f16 v[230:233], v[150:153], a[160:167], v210
	v_mul_f32_e32 v239, v239, v198
	v_smfmac_f32_16x16x64_f16 v[234:237], v[150:153], v[98:105], v210
	v_fmac_f32_e32 v219, v239, v239
	v_smfmac_f32_16x16x64_f16 v[230:233], v[154:157], a[192:199], v210
	ds_read_b128 v[238:241], v217
	v_smfmac_f32_16x16x64_f16 v[234:237], v[154:157], v[106:113], v210
	ds_read_b128 v[242:245], v217
	v_smfmac_f32_16x16x64_f16 v[230:233], v[158:161], a[224:231], v210
	v_smfmac_f32_16x16x64_f16 v[234:237], v[158:161], v[122:129], v210
	s_waitcnt lgkmcnt(1)
	v_smfmac_f32_16x16x64_f16 v[238:241], v[130:133], a[8:15], v210
	s_waitcnt lgkmcnt(0)
	v_smfmac_f32_16x16x64_f16 v[242:245], v[130:133], v[2:9], v210
	v_smfmac_f32_16x16x64_f16 v[238:241], v[134:137], a[32:39], v210
	v_fmac_f32_e32 v230, s40, v231
	v_smfmac_f32_16x16x64_f16 v[242:245], v[134:137], v[10:17], v210
	v_fmac_f32_e32 v234, s40, v235
	v_smfmac_f32_16x16x64_f16 v[238:241], v[138:141], a[72:79], v210
	v_fmac_f32_e32 v230, s41, v232
	v_smfmac_f32_16x16x64_f16 v[242:245], v[138:141], v[50:57], v210
	v_fmac_f32_e32 v234, s41, v236
	v_smfmac_f32_16x16x64_f16 v[238:241], v[142:145], a[104:111], v210
	s_nop 0
	v_permlane32_swap_b32_e32 v230, v234
	v_smfmac_f32_16x16x64_f16 v[242:245], v[142:145], v[26:33], v210
	v_add_f32_e32 v166, v230, v234
	v_smfmac_f32_16x16x64_f16 v[238:241], v[146:149], a[136:143], v210
	v_fmac_f32_e32 v162, 0xbccccccd, v166
	v_smfmac_f32_16x16x64_f16 v[242:245], v[146:149], v[82:89], v210
	v_mul_f32_e32 v231, v178, v162
	v_smfmac_f32_16x16x64_f16 v[238:241], v[150:153], a[168:175], v210
	v_mul_f32_e32 v231, v231, v179
	v_smfmac_f32_16x16x64_f16 v[242:245], v[150:153], v[66:73], v210
	v_fmac_f32_e32 v219, v231, v231
	v_smfmac_f32_16x16x64_f16 v[238:241], v[154:157], a[200:207], v210
	ds_read_b128 v[230:233], v217
	v_smfmac_f32_16x16x64_f16 v[242:245], v[154:157], v[114:121], v210
	ds_read_b128 v[234:237], v217
	v_smfmac_f32_16x16x64_f16 v[238:241], v[158:161], a[232:239], v210
	v_smfmac_f32_16x16x64_f16 v[242:245], v[158:161], v[90:97], v210
	s_nop 6
	v_fmac_f32_e32 v238, s40, v239
	v_fmac_f32_e32 v242, s40, v243
	v_fmac_f32_e32 v238, s41, v240
	v_fmac_f32_e32 v242, s41, v244
	s_nop 1
	v_permlane32_swap_b32_e32 v238, v242
	v_add_f32_e32 v167, v238, v242
	v_fmac_f32_e32 v163, 0xbccccccd, v167
	v_mul_f32_e32 v239, v178, v163
	v_mul_f32_e32 v239, v239, v196
	v_fmac_f32_e32 v219, v239, v239
	ds_read_b128 v[180:183], v199 offset:0
	ds_read_b128 v[184:187], v199 offset:1024
	ds_read_b128 v[188:191], v199 offset:4096
	ds_read_b128 v[192:195], v199 offset:5120
	ds_read_b128 v[222:225], v199 offset:8192
	ds_read_b128 v[226:229], v199 offset:9216
	v_add_f32_dpp v238, v219, v219 quad_perm:[1,0,3,2] row_mask:0xf bank_mask:0xf bound_ctrl:1
	s_nop 1
	v_add_f32_dpp v238, v238, v238 quad_perm:[2,3,0,1] row_mask:0xf bank_mask:0xf bound_ctrl:1
	s_nop 1
	v_add_f32_dpp v238, v238, v238 row_half_mirror row_mask:0xf bank_mask:0xf bound_ctrl:1
	s_nop 1
	v_add_f32_dpp v238, v238, v238 row_mirror row_mask:0xf bank_mask:0xf bound_ctrl:1
	v_mov_b32_e32 v239, v238
	s_nop 1
	v_permlane32_swap_b32_e32 v238, v239
	v_add_f32_e32 v238, v238, v239
	v_lshl_add_u32 v240, s29, 6, v218
	v_lshlrev_b32_e32 v241, 3, v201
	v_or_b32_e32 v241, 0x24400, v241
	v_lshl_add_u32 v241, s29, 6, v241
	s_and_saveexec_b64 s[2:3], s[4:5]
	ds_write_b32 v240, v238
	s_or_b64 exec, exec, s[2:3]
	s_waitcnt lgkmcnt(0)
	s_barrier
	ds_read2_b32 v[130:131], v241 offset1:4
	ds_read2_b32 v[132:133], v241 offset0:8 offset1:12
	s_waitcnt lgkmcnt(1)
	v_add_f32_e32 v238, v130, v131
	s_waitcnt lgkmcnt(0)
	v_add_f32_e32 v238, v238, v132
	v_add_f32_e32 v238, v238, v133
	v_mul_f32_e32 v238, 0x3b000000, v238
	v_max_f32_e32 v238, 0xda24260, v238
	v_sqrt_f32_e32 v238, v238
	s_nop 0
	v_cmp_ngt_f32_e64 s[2:3], 1.0, v238
	v_cmp_gt_f32_e32 vcc, 1.0, v238
	v_log_f32_e32 v239, v238
	v_mul_f32_e32 v241, 0x44000000, v178
	s_and_saveexec_b64 s[26:27], vcc
	v_add_f32_e32 v221, v221, v241
	v_mov_b32_e32 v171, v252
	v_mov_b32_e32 v173, v166
	v_mov_b32_e32 v170, v253
	v_mov_b32_e32 v172, v167
	v_mov_b32_e32 v169, v254
	v_mov_b32_e32 v175, v176
	v_mov_b32_e32 v168, v255
	v_mov_b32_e32 v174, v177
	s_or_b64 exec, exec, s[26:27]
	v_mov_b32_e32 v240, 0x41200000
	s_nop 0
	v_cndmask_b32_e64 v240, v240, 1.0, s[22:23]
	s_xor_b32 s29, s29, 1
	s_add_i32 s30, s30, 1
	v_mul_f32_e32 v239, 0xbe4ccccd, v239
	v_exp_f32_e32 v239, v239
	s_nop 0
	v_mul_f32_e32 v239, 0x3f666666, v239
	v_min_f32_e32 v240, v239, v240
	v_max_f32_e32 v239, 0x3e4ccccd, v239
	v_cndmask_b32_e64 v239, v240, v239, s[2:3]
	v_mul_f32_e32 v1, v241, v239
	s_mov_b64 s[22:23], s[2:3]
	s_branch .Lrk_top
